# Deferred expert-weight conversion: converted bf16 weights stored with the nt hint (consumed hundreds of microseconds later by other XCDs; keeps them from displacing GEMM tiles in L2)
# speedup vs baseline: 1.0118x; 1.0002x over previous
; __device__ __forceinline__ unsigned cvt_pk_bf16(float lo, float hi) { f32x2_t v = {lo, hi}; bf16x2_t b = __builtin_convertvector(v, bf16x2_t); return __builtin_bit_cast(unsigned, b); }
; __device__ __forceinline__ void conv_span128(const float* W, int ldw, int K, bf16* WT, int rowmode, int kb, int n0, int lane) {
;     const int c = lane & 7, nn = lane >> 3;
;     const float* src = W + (size_t)(kb * 64 + 8 * c) * ldw + n0 + 4 * nn;
;     f32x4 v[4][8];
; #pragma unroll
;     for (int h = 0; h < 4; ++h)
; #pragma unroll
;         for (int i = 0; i < 8; ++i) v[h][i] = __builtin_nontemporal_load((const f32x4*)(src + 32 * h + (size_t)i * ldw));
; #pragma unroll
;     for (int h = 0; h < 4; ++h) {
;         const int n = n0 + 32 * h + 4 * nn; int r = n;
;         if (rowmode == 2) r = ((n >> 7) << 8) + (n & 127);
;         else if (rowmode == 3) r = ((n >> 7) << 8) + 128 + (n & 127);
;         bf16* d0 = WT + (size_t)r * K + kb * 64 + 8 * c;
; #pragma unroll
;         for (int j = 0; j < 4; ++j) { u32x4 o; o.x = cvt_pk_bf16(v[h][0][j], v[h][1][j]); o.y = cvt_pk_bf16(v[h][2][j], v[h][3][j]); o.z = cvt_pk_bf16(v[h][4][j], v[h][5][j]); o.w = cvt_pk_bf16(v[h][6][j], v[h][7][j]);
;             *(u32x4*)(d0 + (size_t)j * K) = o; }
;     }
; }
;     ...
;         else { const int e = p / 224, q = p % 224, kb = q >> 1, h = kb / 56;
;             conv_span128(m2 + (size_t)e * FFE * D + (size_t)h * (FFE / 2) * D, 2048, FFE / 2, mdn + (size_t)(e * 2 + h) * D * (FFE / 2), 0, kb - 56 * h, (q & 1) * 1024 + wave * 128, lane); }
.LBB0_151:
	s_or_b64 exec, exec, s[6:7]
	s_and_b32 s8, s20, 0x7fffffff
	s_cmp_lt_i32 s20, 0
	s_mov_b64 s[6:7], -1
	s_cbranch_scc0 .LBB0_153
	s_lshr_b32 s6, s8, 5
	s_mul_hi_u32 s9, s6, 0x24924925
	s_mul_i32 s6, s9, 0xe0
	s_sub_i32 s12, s8, s6
	s_lshr_b32 s13, s12, 1
	s_cmpk_gt_u32 s12, 0x6f
	s_mul_i32 s11, s9, 0x3800000
	v_readlane_b32 s40, v255, 3
	s_cselect_b64 s[6:7], -1, 0
	s_mul_hi_u32 s10, s9, 0x3800000
	v_readlane_b32 s41, v255, 4
	s_add_u32 s14, s40, s11
	s_addc_u32 s15, s41, s10
	s_and_b64 s[10:11], s[6:7], exec
	s_cselect_b32 s10, 0x1c00000, 0
	v_cndmask_b32_e64 v2, 0, 1, s[6:7]
	s_add_u32 s10, s14, s10
	s_addc_u32 s11, s15, 0
	s_lshl_b32 s9, s9, 1
	v_readfirstlane_b32 s14, v2
	s_or_b32 s9, s9, s14
	s_mul_hi_u32 s14, s9, 0xe00000
	s_mul_i32 s9, s9, 0xe00000
	v_readlane_b32 s15, v250, 16
	s_add_u32 s9, s15, s9
	v_readlane_b32 s15, v250, 17
	s_addc_u32 s14, s15, s14
	s_and_b64 s[6:7], s[6:7], exec
	s_cselect_b32 s6, 0xffffffc8, 0
	s_add_i32 s7, s6, s13
	s_lshl_b32 s6, s12, 10
	s_lshl_b32 s12, s7, 6
	v_or_b32_e32 v2, s12, v126
	s_and_b32 s6, s6, 0x400
	v_ashrrev_i32_e32 v3, 31, v2
	s_add_i32 s6, s6, s18
	v_lshlrev_b64 v[2:3], 13, v[2:3]
	v_lshl_add_u64 v[2:3], s[10:11], 0, v[2:3]
	s_ashr_i32 s7, s6, 31
	v_lshl_add_u64 v[2:3], s[6:7], 2, v[2:3]
	v_mov_b32_e32 v131, v187
	v_lshl_add_u64 v[2:3], v[2:3], 0, v[130:131]
	s_movk_i32 s7, 0x2000
	v_add_co_u32_e32 v6, vcc, s7, v2
	s_movk_i32 s7, 0x4000
	s_nop 0
	v_addc_co_u32_e32 v7, vcc, 0, v3, vcc
	v_add_co_u32_e32 v10, vcc, s7, v2
	s_movk_i32 s7, 0x6000
	s_nop 0
	v_addc_co_u32_e32 v11, vcc, 0, v3, vcc
	v_add_co_u32_e32 v14, vcc, s7, v2
	s_mov_b32 s7, 0x8000
	s_nop 0
	v_addc_co_u32_e32 v15, vcc, 0, v3, vcc
	v_add_co_u32_e32 v18, vcc, s7, v2
	s_mov_b32 s7, 0xa000
	s_nop 0
	v_addc_co_u32_e32 v19, vcc, 0, v3, vcc
	v_add_co_u32_e32 v22, vcc, s7, v2
	s_mov_b32 s7, 0xc000
	s_nop 0
	v_addc_co_u32_e32 v23, vcc, 0, v3, vcc
	v_add_co_u32_e32 v26, vcc, s7, v2
	global_load_dwordx4 v[98:101], v[2:3], off nt
	global_load_dwordx4 v[102:105], v[6:7], off nt
	v_addc_co_u32_e32 v27, vcc, 0, v3, vcc
	global_load_dwordx4 v[106:109], v[10:11], off nt
	global_load_dwordx4 v[110:113], v[14:15], off nt
	global_load_dwordx4 v[114:117], v[18:19], off nt
	global_load_dwordx4 v[118:121], v[22:23], off nt
	global_load_dwordx4 v[122:125], v[26:27], off nt
	s_mov_b32 s7, 0xe000
	v_add_co_u32_e32 v30, vcc, s7, v2
	s_ashr_i32 s13, s12, 31
	s_nop 0
	v_addc_co_u32_e32 v31, vcc, 0, v3, vcc
	global_load_dwordx4 v[134:137], v[30:31], off nt
	global_load_dwordx4 v[66:69], v[2:3], off offset:128 nt
	global_load_dwordx4 v[70:73], v[6:7], off offset:128 nt
	global_load_dwordx4 v[74:77], v[10:11], off offset:128 nt
	global_load_dwordx4 v[78:81], v[14:15], off offset:128 nt
	global_load_dwordx4 v[82:85], v[18:19], off offset:128 nt
	global_load_dwordx4 v[86:89], v[22:23], off offset:128 nt
	global_load_dwordx4 v[90:93], v[26:27], off offset:128 nt
	global_load_dwordx4 v[94:97], v[30:31], off offset:128 nt
	global_load_dwordx4 v[34:37], v[2:3], off offset:256 nt
	global_load_dwordx4 v[38:41], v[6:7], off offset:256 nt
	global_load_dwordx4 v[42:45], v[10:11], off offset:256 nt
	global_load_dwordx4 v[46:49], v[14:15], off offset:256 nt
	global_load_dwordx4 v[50:53], v[18:19], off offset:256 nt
	global_load_dwordx4 v[54:57], v[22:23], off offset:256 nt
	global_load_dwordx4 v[58:61], v[26:27], off offset:256 nt
	global_load_dwordx4 v[62:65], v[30:31], off offset:256 nt
	s_nop 0
	global_load_dwordx4 v[2:5], v[2:3], off offset:384 nt
	s_nop 0
	global_load_dwordx4 v[6:9], v[6:7], off offset:384 nt
	s_nop 0
	global_load_dwordx4 v[10:13], v[10:11], off offset:384 nt
	s_nop 0
	global_load_dwordx4 v[14:17], v[14:15], off offset:384 nt
	s_nop 0
	global_load_dwordx4 v[18:21], v[18:19], off offset:384 nt
	s_nop 0
	global_load_dwordx4 v[22:25], v[22:23], off offset:384 nt
	s_nop 0
	global_load_dwordx4 v[26:29], v[26:27], off offset:384 nt
	s_nop 0
	global_load_dwordx4 v[30:33], v[30:31], off offset:384 nt
	v_or_b32_e32 v131, s6, v128
	s_lshl_b64 s[6:7], s[12:13], 1
	s_add_u32 s6, s9, s6
	s_addc_u32 s7, s14, s7
	v_mov_b32_e32 v133, v187
	v_lshl_add_u64 v[142:143], s[6:7], 0, v[132:133]
	s_movk_i32 s10, 0x1c00
	v_mad_i64_i32 v[144:145], s[6:7], v131, s10, v[142:143]
	s_movk_i32 s9, 0x1000
	s_movk_i32 s11, 0x3000
	s_movk_i32 s12, 0x5000
	v_readlane_b32 s42, v255, 5
	v_readlane_b32 s43, v255, 6
	s_movk_i32 s97, 0x1000
	s_waitcnt vmcnt(0)
	v_cvt_pk_bf16_f32 v138, v98, v102
	v_add_co_u32_e32 v98, vcc, s9, v144
	s_waitcnt vmcnt(28)
	v_cvt_pk_bf16_f32 v139, v106, v110
	s_waitcnt vmcnt(26)
	v_cvt_pk_bf16_f32 v140, v114, v118
	s_waitcnt vmcnt(24)
	v_cvt_pk_bf16_f32 v141, v122, v134
	global_store_dwordx4 v[144:145], v[138:141], off nt
	s_nop 1
	v_cvt_pk_bf16_f32 v138, v99, v103
	v_cvt_pk_bf16_f32 v139, v107, v111
	v_cvt_pk_bf16_f32 v140, v115, v119
	v_cvt_pk_bf16_f32 v141, v123, v135
	v_addc_co_u32_e32 v99, vcc, 0, v145, vcc
	global_store_dwordx4 v[98:99], v[138:141], off offset:3072 nt
	v_add_co_u32_e32 v98, vcc, s11, v144
	s_nop 0
	v_cvt_pk_bf16_f32 v138, v100, v104
	v_addc_co_u32_e32 v99, vcc, 0, v145, vcc
	v_cvt_pk_bf16_f32 v139, v108, v112
	v_cvt_pk_bf16_f32 v140, v116, v120
	v_cvt_pk_bf16_f32 v141, v124, v136
	v_add_co_u32_e32 v102, vcc, s12, v144
	global_store_dwordx4 v[98:99], v[138:141], off offset:2048 nt
	v_cvt_pk_bf16_f32 v98, v101, v105
	v_cvt_pk_bf16_f32 v99, v109, v113
	v_cvt_pk_bf16_f32 v100, v117, v121
	v_cvt_pk_bf16_f32 v101, v125, v137
	v_addc_co_u32_e32 v103, vcc, 0, v145, vcc
	global_store_dwordx4 v[102:103], v[98:101], off offset:1024 nt
	s_nop 1
	v_or_b32_e32 v98, 32, v131
	v_mad_i64_i32 v[102:103], s[6:7], v98, s10, v[142:143]
	s_waitcnt vmcnt(26)
; __device__ __forceinline__ unsigned cvt_pk_bf16(float lo, float hi) { f32x2_t v = {lo, hi}; bf16x2_t b = __builtin_convertvector(v, bf16x2_t); return __builtin_bit_cast(unsigned, b); }
; __device__ __forceinline__ void conv_span128(const float* W, int ldw, int K, bf16* WT, int rowmode, int kb, int n0, int lane) {
;     const int c = lane & 7, nn = lane >> 3;
;     const float* src = W + (size_t)(kb * 64 + 8 * c) * ldw + n0 + 4 * nn;
;     f32x4 v[4][8];
; #pragma unroll
;     for (int h = 0; h < 4; ++h)
; #pragma unroll
;         for (int i = 0; i < 8; ++i) v[h][i] = __builtin_nontemporal_load((const f32x4*)(src + 32 * h + (size_t)i * ldw));
; #pragma unroll
;     for (int h = 0; h < 4; ++h) {
;         const int n = n0 + 32 * h + 4 * nn; int r = n;
;         if (rowmode == 2) r = ((n >> 7) << 8) + (n & 127);
;         else if (rowmode == 3) r = ((n >> 7) << 8) + 128 + (n & 127);
;         bf16* d0 = WT + (size_t)r * K + kb * 64 + 8 * c;
; #pragma unroll
;         for (int j = 0; j < 4; ++j) { u32x4 o; o.x = cvt_pk_bf16(v[h][0][j], v[h][1][j]); o.y = cvt_pk_bf16(v[h][2][j], v[h][3][j]); o.z = cvt_pk_bf16(v[h][4][j], v[h][5][j]); o.w = cvt_pk_bf16(v[h][6][j], v[h][7][j]);
;             *(u32x4*)(d0 + (size_t)j * K) = o; }
;     }
; }
;     ...
;         if ((cur >> 31) == 0u) { const int e = p / 448, w3 = (p / 224) & 1, q = p % 224;
;             conv_span128((w3 ? m3 : m1) + (size_t)e * D * FFE, FFE, D, mup + (size_t)e * 2 * FFE * D, 2 + w3, q / 7, (q % 7) * 1024 + wave * 128, lane); }
	v_cvt_pk_bf16_f32 v98, v66, v70
	s_waitcnt vmcnt(24)
	v_cvt_pk_bf16_f32 v99, v74, v78
	s_waitcnt vmcnt(22)
	v_cvt_pk_bf16_f32 v100, v82, v86
	s_waitcnt vmcnt(20)
	v_cvt_pk_bf16_f32 v101, v90, v94
	v_add_co_u32_e32 v66, vcc, s9, v102
	global_store_dwordx4 v[102:103], v[98:101], off nt
	s_nop 1
	v_cvt_pk_bf16_f32 v98, v67, v71
	v_cvt_pk_bf16_f32 v99, v75, v79
	v_cvt_pk_bf16_f32 v100, v83, v87
	v_cvt_pk_bf16_f32 v101, v91, v95
	v_addc_co_u32_e32 v67, vcc, 0, v103, vcc
	global_store_dwordx4 v[66:67], v[98:101], off offset:3072 nt
	v_add_co_u32_e32 v66, vcc, s11, v102
	s_nop 0
	v_cvt_pk_bf16_f32 v98, v68, v72
	v_addc_co_u32_e32 v67, vcc, 0, v103, vcc
	v_cvt_pk_bf16_f32 v99, v76, v80
	v_cvt_pk_bf16_f32 v100, v84, v88
	v_cvt_pk_bf16_f32 v101, v92, v96
	v_add_co_u32_e32 v70, vcc, s12, v102
	global_store_dwordx4 v[66:67], v[98:101], off offset:2048 nt
	v_cvt_pk_bf16_f32 v66, v69, v73
	v_cvt_pk_bf16_f32 v67, v77, v81
	v_cvt_pk_bf16_f32 v68, v85, v89
	v_cvt_pk_bf16_f32 v69, v93, v97
	v_addc_co_u32_e32 v71, vcc, 0, v103, vcc
	global_store_dwordx4 v[70:71], v[66:69], off offset:1024 nt
	s_nop 1
	v_or_b32_e32 v66, 64, v131
	v_mad_i64_i32 v[70:71], s[6:7], v66, s10, v[142:143]
	s_waitcnt vmcnt(22)
	v_cvt_pk_bf16_f32 v66, v34, v38
	s_waitcnt vmcnt(20)
	v_cvt_pk_bf16_f32 v67, v42, v46
	s_waitcnt vmcnt(18)
	v_cvt_pk_bf16_f32 v68, v50, v54
	s_waitcnt vmcnt(16)
	v_cvt_pk_bf16_f32 v69, v58, v62
	v_add_co_u32_e32 v34, vcc, s9, v70
	global_store_dwordx4 v[70:71], v[66:69], off nt
	s_nop 1
	v_cvt_pk_bf16_f32 v66, v35, v39
	v_cvt_pk_bf16_f32 v67, v43, v47
	v_cvt_pk_bf16_f32 v68, v51, v55
	v_cvt_pk_bf16_f32 v69, v59, v63
	v_addc_co_u32_e32 v35, vcc, 0, v71, vcc
	global_store_dwordx4 v[34:35], v[66:69], off offset:3072 nt
	v_add_co_u32_e32 v34, vcc, s11, v70
	s_nop 0
	v_cvt_pk_bf16_f32 v66, v36, v40
	v_addc_co_u32_e32 v35, vcc, 0, v71, vcc
	v_cvt_pk_bf16_f32 v67, v44, v48
	v_cvt_pk_bf16_f32 v68, v52, v56
	v_cvt_pk_bf16_f32 v69, v60, v64
	v_add_co_u32_e32 v38, vcc, s12, v70
	global_store_dwordx4 v[34:35], v[66:69], off offset:2048 nt
	v_cvt_pk_bf16_f32 v34, v37, v41
	v_cvt_pk_bf16_f32 v35, v45, v49
	v_cvt_pk_bf16_f32 v36, v53, v57
	v_cvt_pk_bf16_f32 v37, v61, v65
	v_addc_co_u32_e32 v39, vcc, 0, v71, vcc
	global_store_dwordx4 v[38:39], v[34:37], off offset:1024 nt
	s_nop 1
	v_or_b32_e32 v34, 0x60, v131
	v_mad_i64_i32 v[38:39], s[6:7], v34, s10, v[142:143]
	s_waitcnt vmcnt(18)
	v_cvt_pk_bf16_f32 v34, v2, v6
	s_waitcnt vmcnt(16)
	v_cvt_pk_bf16_f32 v35, v10, v14
	s_waitcnt vmcnt(14)
	v_cvt_pk_bf16_f32 v36, v18, v22
	s_waitcnt vmcnt(12)
	v_cvt_pk_bf16_f32 v37, v26, v30
	v_add_co_u32_e32 v2, vcc, s9, v38
	global_store_dwordx4 v[38:39], v[34:37], off nt
	s_mov_b64 s[6:7], 0
	s_nop 0
	v_cvt_pk_bf16_f32 v34, v3, v7
	v_cvt_pk_bf16_f32 v35, v11, v15
	v_cvt_pk_bf16_f32 v36, v19, v23
	v_cvt_pk_bf16_f32 v37, v27, v31
	v_addc_co_u32_e32 v3, vcc, 0, v39, vcc
	global_store_dwordx4 v[2:3], v[34:37], off offset:3072 nt
	v_add_co_u32_e32 v2, vcc, s11, v38
	s_nop 0
	v_cvt_pk_bf16_f32 v34, v4, v8
	v_addc_co_u32_e32 v3, vcc, 0, v39, vcc
	v_cvt_pk_bf16_f32 v35, v12, v16
	v_cvt_pk_bf16_f32 v36, v20, v24
	v_cvt_pk_bf16_f32 v37, v28, v32
	v_add_co_u32_e32 v6, vcc, 0x5000, v38
	global_store_dwordx4 v[2:3], v[34:37], off offset:2048 nt
	v_cvt_pk_bf16_f32 v2, v5, v9
	v_cvt_pk_bf16_f32 v3, v13, v17
	v_cvt_pk_bf16_f32 v4, v21, v25
	v_cvt_pk_bf16_f32 v5, v29, v33
	v_addc_co_u32_e32 v7, vcc, 0, v39, vcc
	global_store_dwordx4 v[6:7], v[2:5], off offset:1024 nt
.LBB0_153:
	s_andn2_b64 vcc, exec, s[6:7]
	s_cbranch_vccnz .LBB0_135
	s_lshr_b32 s7, s20, 5
	s_mul_hi_u32 s7, s7, 0x24924925
	s_and_b32 s12, s7, 1
	s_mul_hi_u32 s7, s8, 0x92492493
	s_lshr_b32 s7, s7, 7
	s_mulk_i32 s7, 0xe0
	s_lshr_b32 s6, s20, 6
	s_sub_i32 s10, s8, s7
	v_readlane_b32 s40, v255, 7
	s_mul_hi_u32 s6, s6, 0x24924925
	s_cmp_eq_u32 s12, 0
	v_readlane_b32 s44, v255, 11
	v_readlane_b32 s46, v255, 13
	v_readlane_b32 s45, v255, 12
	v_readlane_b32 s47, v255, 14
	s_cselect_b32 s8, s44, s46
	s_mul_hi_u32 s11, s6, 0x3800000
	s_mul_i32 s13, s6, 0x3800000
	s_movk_i32 s6, 0x60
	s_cselect_b32 s9, s45, s47
	s_cselect_b32 s14, 32, 0xa0
	s_cselect_b32 s7, 64, 0xc0
	s_cselect_b32 s6, s6, 0xe0
	s_add_u32 s8, s8, s13
	s_addc_u32 s9, s9, s11
	v_readlane_b32 s15, v250, 14
	s_add_u32 s13, s15, s13
	v_readlane_b32 s15, v250, 15
	s_addc_u32 s11, s15, s11
	s_and_b32 s15, s10, 0xff
	s_mul_i32 s15, s15, 37
	s_lshr_b32 s15, s15, 8
	s_sub_i32 s16, s10, s15
	s_bfe_u32 s16, s16, 0x70001
	s_add_i32 s16, s16, s15
	s_bfe_u32 s15, s16, 0x60002
	v_lshl_or_b32 v2, s15, 6, v126
	s_mul_i32 s16, s15, 7
	v_mul_u32_u24_e32 v186, 0x1c00, v2
	v_lshl_add_u64 v[2:3], v[186:187], 2, s[8:9]
	s_sub_i32 s8, s10, s16
	s_and_b32 s8, s8, 0xff
	s_lshl_b32 s8, s8, 10
	s_add_i32 s8, s8, s18
	s_ashr_i32 s9, s8, 31
	v_lshl_add_u64 v[2:3], s[8:9], 2, v[2:3]
	v_mov_b32_e32 v131, v187
	v_lshl_add_u64 v[70:71], v[2:3], 0, v[130:131]
	s_movk_i32 s9, 0x7000
	v_add_co_u32_e32 v78, vcc, s9, v70
	s_mov_b32 s9, 0xe000
	s_nop 0
	v_addc_co_u32_e32 v79, vcc, 0, v71, vcc
	v_add_co_u32_e32 v86, vcc, s9, v70
	s_mov_b32 s9, 0x15000
	s_nop 0
	v_addc_co_u32_e32 v87, vcc, 0, v71, vcc
	v_add_co_u32_e32 v94, vcc, s9, v70
	s_mov_b32 s9, 0x1c000
	s_nop 0
	v_addc_co_u32_e32 v95, vcc, 0, v71, vcc
	v_add_co_u32_e32 v102, vcc, s9, v70
	s_mov_b32 s9, 0x23000
	s_nop 0
	v_addc_co_u32_e32 v103, vcc, 0, v71, vcc
	v_add_co_u32_e32 v110, vcc, s9, v70
	s_mov_b32 s9, 0x2a000
	s_nop 0
	v_addc_co_u32_e32 v111, vcc, 0, v71, vcc
	v_add_co_u32_e32 v118, vcc, s9, v70
	global_load_dwordx4 v[2:5], v[70:71], off nt
	global_load_dwordx4 v[6:9], v[78:79], off nt
	v_addc_co_u32_e32 v119, vcc, 0, v71, vcc
	global_load_dwordx4 v[10:13], v[86:87], off nt
; __device__ __forceinline__ unsigned cvt_pk_bf16(float lo, float hi) { f32x2_t v = {lo, hi}; bf16x2_t b = __builtin_convertvector(v, bf16x2_t); return __builtin_bit_cast(unsigned, b); }
; __device__ __forceinline__ void conv_span128(const float* W, int ldw, int K, bf16* WT, int rowmode, int kb, int n0, int lane) {
;     const int c = lane & 7, nn = lane >> 3;
;     const float* src = W + (size_t)(kb * 64 + 8 * c) * ldw + n0 + 4 * nn;
;     f32x4 v[4][8];
; #pragma unroll
;     for (int h = 0; h < 4; ++h)
; #pragma unroll
;         for (int i = 0; i < 8; ++i) v[h][i] = __builtin_nontemporal_load((const f32x4*)(src + 32 * h + (size_t)i * ldw));
; #pragma unroll
;     for (int h = 0; h < 4; ++h) {
;         const int n = n0 + 32 * h + 4 * nn; int r = n;
;         if (rowmode == 2) r = ((n >> 7) << 8) + (n & 127);
;         else if (rowmode == 3) r = ((n >> 7) << 8) + 128 + (n & 127);
;         bf16* d0 = WT + (size_t)r * K + kb * 64 + 8 * c;
; #pragma unroll
;         for (int j = 0; j < 4; ++j) { u32x4 o; o.x = cvt_pk_bf16(v[h][0][j], v[h][1][j]); o.y = cvt_pk_bf16(v[h][2][j], v[h][3][j]); o.z = cvt_pk_bf16(v[h][4][j], v[h][5][j]); o.w = cvt_pk_bf16(v[h][6][j], v[h][7][j]);
;             *(u32x4*)(d0 + (size_t)j * K) = o; }
;     }
; }
	global_load_dwordx4 v[14:17], v[94:95], off nt
	global_load_dwordx4 v[18:21], v[102:103], off nt
	global_load_dwordx4 v[22:25], v[110:111], off nt
	global_load_dwordx4 v[26:29], v[118:119], off nt
	s_mov_b32 s9, 0x31000
	v_add_co_u32_e32 v134, vcc, s9, v70
	s_lshl_b32 s9, s15, 7
	s_nop 0
	v_addc_co_u32_e32 v135, vcc, 0, v71, vcc
	global_load_dwordx4 v[30:33], v[134:135], off nt
	global_load_dwordx4 v[34:37], v[70:71], off offset:128 nt
	global_load_dwordx4 v[38:41], v[78:79], off offset:128 nt
	global_load_dwordx4 v[42:45], v[86:87], off offset:128 nt
	global_load_dwordx4 v[46:49], v[94:95], off offset:128 nt
	global_load_dwordx4 v[50:53], v[102:103], off offset:128 nt
	global_load_dwordx4 v[54:57], v[110:111], off offset:128 nt
	global_load_dwordx4 v[58:61], v[118:119], off offset:128 nt
	global_load_dwordx4 v[62:65], v[134:135], off offset:128 nt
	global_load_dwordx4 v[66:69], v[70:71], off offset:256 nt
	s_nop 0
	global_load_dwordx4 v[70:73], v[70:71], off offset:384 nt
	s_nop 0
	global_load_dwordx4 v[74:77], v[78:79], off offset:256 nt
	s_nop 0
	global_load_dwordx4 v[78:81], v[78:79], off offset:384 nt
	s_nop 0
	global_load_dwordx4 v[82:85], v[86:87], off offset:256 nt
	s_nop 0
	global_load_dwordx4 v[86:89], v[86:87], off offset:384 nt
	s_nop 0
	global_load_dwordx4 v[90:93], v[94:95], off offset:256 nt
	s_nop 0
	global_load_dwordx4 v[94:97], v[94:95], off offset:384 nt
	s_nop 0
	global_load_dwordx4 v[98:101], v[102:103], off offset:256 nt
	s_nop 0
	global_load_dwordx4 v[102:105], v[102:103], off offset:384 nt
	s_nop 0
	global_load_dwordx4 v[106:109], v[110:111], off offset:256 nt
	s_nop 0
	global_load_dwordx4 v[110:113], v[110:111], off offset:384 nt
	s_nop 0
	global_load_dwordx4 v[114:117], v[118:119], off offset:256 nt
	s_nop 0
	global_load_dwordx4 v[118:121], v[118:119], off offset:384 nt
	s_nop 0
	global_load_dwordx4 v[122:125], v[134:135], off offset:256 nt
	s_nop 0
	global_load_dwordx4 v[134:137], v[134:135], off offset:384 nt
	s_add_u32 s10, s13, s9
	s_addc_u32 s11, s11, 0
	s_lshl_b32 s8, s8, 1
	v_lshl_or_b32 v131, s12, 7, v128
	v_or_b32_e32 v138, s8, v131
	v_mov_b32_e32 v133, v187
	v_ashrrev_i32_e32 v139, 31, v138
	v_lshl_add_u64 v[142:143], s[10:11], 0, v[132:133]
	v_lshlrev_b64 v[138:139], 12, v[138:139]
	v_lshl_add_u64 v[144:145], v[142:143], 0, v[138:139]
	s_movk_i32 s9, 0x2000
	s_movk_i32 s10, 0x3000
	v_readlane_b32 s41, v255, 8
	v_readlane_b32 s42, v255, 9
	v_readlane_b32 s43, v255, 10
	s_waitcnt vmcnt(0)
	v_cvt_pk_bf16_f32 v138, v2, v6
	v_add_co_u32_e32 v2, vcc, s9, v144
	s_waitcnt vmcnt(28)
	v_cvt_pk_bf16_f32 v139, v10, v14
	s_waitcnt vmcnt(26)
	v_cvt_pk_bf16_f32 v140, v18, v22
	s_waitcnt vmcnt(24)
	v_cvt_pk_bf16_f32 v141, v26, v30
	global_store_dwordx4 v[144:145], v[138:141], off nt
	s_nop 1
	v_cvt_pk_bf16_f32 v138, v3, v7
	v_cvt_pk_bf16_f32 v139, v11, v15
	v_cvt_pk_bf16_f32 v140, v19, v23
	v_cvt_pk_bf16_f32 v141, v27, v31
	v_addc_co_u32_e32 v3, vcc, 0, v145, vcc
	global_store_dwordx4 v[2:3], v[138:141], off offset:-4096 nt
	v_add_co_u32_e32 v6, vcc, s10, v144
	s_nop 0
	v_cvt_pk_bf16_f32 v138, v4, v8
	v_cvt_pk_bf16_f32 v139, v12, v16
	v_cvt_pk_bf16_f32 v140, v20, v24
	v_cvt_pk_bf16_f32 v141, v28, v32
	global_store_dwordx4 v[2:3], v[138:141], off nt
	v_cvt_pk_bf16_f32 v2, v5, v9
	v_cvt_pk_bf16_f32 v3, v13, v17
	v_cvt_pk_bf16_f32 v4, v21, v25
	v_cvt_pk_bf16_f32 v5, v29, v33
	v_addc_co_u32_e32 v7, vcc, 0, v145, vcc
	global_store_dwordx4 v[6:7], v[2:5], off nt
	s_nop 1
	v_or_b32_e32 v2, s14, v128
	v_or_b32_e32 v2, s8, v2
	v_ashrrev_i32_e32 v3, 31, v2
	v_lshlrev_b64 v[2:3], 12, v[2:3]
	v_lshl_add_u64 v[6:7], v[142:143], 0, v[2:3]
	s_waitcnt vmcnt(26)
	v_cvt_pk_bf16_f32 v2, v34, v38
	s_waitcnt vmcnt(24)
	v_cvt_pk_bf16_f32 v3, v42, v46
	s_waitcnt vmcnt(22)
	v_cvt_pk_bf16_f32 v4, v50, v54
	s_waitcnt vmcnt(20)
	v_cvt_pk_bf16_f32 v5, v58, v62
	v_add_co_u32_e32 v8, vcc, s9, v6
	global_store_dwordx4 v[6:7], v[2:5], off nt
	s_nop 0
	v_addc_co_u32_e32 v9, vcc, 0, v7, vcc
	v_cvt_pk_bf16_f32 v2, v35, v39
	v_cvt_pk_bf16_f32 v3, v43, v47
	v_cvt_pk_bf16_f32 v4, v51, v55
	v_cvt_pk_bf16_f32 v5, v59, v63
	global_store_dwordx4 v[8:9], v[2:5], off offset:-4096 nt
	v_add_co_u32_e32 v6, vcc, s10, v6
	s_nop 0
	v_cvt_pk_bf16_f32 v2, v36, v40
	v_cvt_pk_bf16_f32 v3, v44, v48
	v_cvt_pk_bf16_f32 v4, v52, v56
	v_cvt_pk_bf16_f32 v5, v60, v64
	global_store_dwordx4 v[8:9], v[2:5], off nt
	v_addc_co_u32_e32 v7, vcc, 0, v7, vcc
	s_nop 0
	v_cvt_pk_bf16_f32 v2, v37, v41
	v_cvt_pk_bf16_f32 v3, v45, v49
	v_cvt_pk_bf16_f32 v4, v53, v57
	v_cvt_pk_bf16_f32 v5, v61, v65
	global_store_dwordx4 v[6:7], v[2:5], off nt
	s_nop 1
	v_or_b32_e32 v2, s7, v128
	v_or_b32_e32 v2, s8, v2
	v_ashrrev_i32_e32 v3, 31, v2
	v_lshlrev_b64 v[2:3], 12, v[2:3]
	v_lshl_add_u64 v[6:7], v[142:143], 0, v[2:3]
	s_waitcnt vmcnt(21)
	v_cvt_pk_bf16_f32 v2, v66, v74
	s_waitcnt vmcnt(17)
	v_cvt_pk_bf16_f32 v3, v82, v90
	s_waitcnt vmcnt(13)
	v_cvt_pk_bf16_f32 v4, v98, v106
	s_waitcnt vmcnt(9)
	v_cvt_pk_bf16_f32 v5, v114, v122
	v_add_co_u32_e32 v8, vcc, s9, v6
	global_store_dwordx4 v[6:7], v[2:5], off nt
	s_nop 0
	v_addc_co_u32_e32 v9, vcc, 0, v7, vcc
	v_cvt_pk_bf16_f32 v2, v67, v75
	v_cvt_pk_bf16_f32 v3, v83, v91
	v_cvt_pk_bf16_f32 v4, v99, v107
	v_cvt_pk_bf16_f32 v5, v115, v123
	global_store_dwordx4 v[8:9], v[2:5], off offset:-4096 nt
	v_add_co_u32_e32 v6, vcc, s10, v6
	s_nop 0
	v_cvt_pk_bf16_f32 v2, v68, v76
	v_cvt_pk_bf16_f32 v3, v84, v92
	v_cvt_pk_bf16_f32 v4, v100, v108
	v_cvt_pk_bf16_f32 v5, v116, v124
	global_store_dwordx4 v[8:9], v[2:5], off nt
	v_addc_co_u32_e32 v7, vcc, 0, v7, vcc
	s_nop 0
	v_cvt_pk_bf16_f32 v2, v69, v77
	v_cvt_pk_bf16_f32 v3, v85, v93
	v_cvt_pk_bf16_f32 v4, v101, v109
	v_cvt_pk_bf16_f32 v5, v117, v125
	global_store_dwordx4 v[6:7], v[2:5], off nt
	s_nop 1
	v_or_b32_e32 v2, s6, v128
	v_or_b32_e32 v2, s8, v2
	v_ashrrev_i32_e32 v3, 31, v2
	v_lshlrev_b64 v[2:3], 12, v[2:3]
	v_lshl_add_u64 v[6:7], v[142:143], 0, v[2:3]
	v_cvt_pk_bf16_f32 v2, v70, v78
	v_cvt_pk_bf16_f32 v3, v86, v94
	v_cvt_pk_bf16_f32 v4, v102, v110
	s_waitcnt vmcnt(12)
	v_cvt_pk_bf16_f32 v5, v118, v134
	v_add_co_u32_e32 v8, vcc, s9, v6
	global_store_dwordx4 v[6:7], v[2:5], off nt
	s_nop 0
	v_addc_co_u32_e32 v9, vcc, 0, v7, vcc
	v_cvt_pk_bf16_f32 v2, v71, v79
	v_cvt_pk_bf16_f32 v3, v87, v95
	v_cvt_pk_bf16_f32 v4, v103, v111
	v_cvt_pk_bf16_f32 v5, v119, v135
	global_store_dwordx4 v[8:9], v[2:5], off offset:-4096 nt
	v_add_co_u32_e32 v6, vcc, 0x3000, v6
	s_nop 0
	v_cvt_pk_bf16_f32 v2, v72, v80
	v_cvt_pk_bf16_f32 v3, v88, v96
	v_cvt_pk_bf16_f32 v4, v104, v112
	v_cvt_pk_bf16_f32 v5, v120, v136
	global_store_dwordx4 v[8:9], v[2:5], off nt
	v_addc_co_u32_e32 v7, vcc, 0, v7, vcc
	s_nop 0
	v_cvt_pk_bf16_f32 v2, v73, v81
	v_cvt_pk_bf16_f32 v3, v89, v97
	v_cvt_pk_bf16_f32 v4, v105, v113
	v_cvt_pk_bf16_f32 v5, v121, v137
	global_store_dwordx4 v[6:7], v[2:5], off nt
	s_branch .LBB0_135

; __device__ __forceinline__ unsigned cvt_pk_bf16(float lo, float hi) { f32x2_t v = {lo, hi}; bf16x2_t b = __builtin_convertvector(v, bf16x2_t); return __builtin_bit_cast(unsigned, b); }
; __device__ __forceinline__ void conv_span128(const float* W, int ldw, int K, bf16* WT, int rowmode, int kb, int n0, int lane) {
;     const int c = lane & 7, nn = lane >> 3;
;     const float* src = W + (size_t)(kb * 64 + 8 * c) * ldw + n0 + 4 * nn;
;     f32x4 v[4][8];
; #pragma unroll
;     for (int h = 0; h < 4; ++h)
; #pragma unroll
;         for (int i = 0; i < 8; ++i) v[h][i] = __builtin_nontemporal_load((const f32x4*)(src + 32 * h + (size_t)i * ldw));
; #pragma unroll
;     for (int h = 0; h < 4; ++h) {
;         const int n = n0 + 32 * h + 4 * nn; int r = n;
;         if (rowmode == 2) r = ((n >> 7) << 8) + (n & 127);
;         else if (rowmode == 3) r = ((n >> 7) << 8) + 128 + (n & 127);
;         bf16* d0 = WT + (size_t)r * K + kb * 64 + 8 * c;
; #pragma unroll
;         for (int j = 0; j < 4; ++j) { u32x4 o; o.x = cvt_pk_bf16(v[h][0][j], v[h][1][j]); o.y = cvt_pk_bf16(v[h][2][j], v[h][3][j]); o.z = cvt_pk_bf16(v[h][4][j], v[h][5][j]); o.w = cvt_pk_bf16(v[h][6][j], v[h][7][j]);
;             *(u32x4*)(d0 + (size_t)j * K) = o; }
;     }
; }
;     ...
;         else { const int e = p / 224, q = p % 224, kb = q >> 1, h = kb / 56;
;             conv_span128(m2 + (size_t)e * FFE * D + (size_t)h * (FFE / 2) * D, 2048, FFE / 2, mdn + (size_t)(e * 2 + h) * D * (FFE / 2), 0, kb - 56 * h, (q & 1) * 1024 + wave * 128, lane); }
.LBB0_279:
	s_or_b64 exec, exec, s[4:5]
	s_and_b32 s6, s19, 0x7fffffff
	s_mov_b64 s[4:5], -1
	s_cmp_lt_i32 s19, 0
	v_lshlrev_b32_e32 v132, 2, v128
	v_lshlrev_b32_e32 v130, 1, v126
	s_cbranch_scc0 .LBB0_281
	s_lshr_b32 s4, s6, 5
	s_mul_hi_u32 s7, s4, 0x24924925
	s_mul_i32 s4, s7, 0xe0
	s_sub_i32 s10, s6, s4
	s_lshr_b32 s11, s10, 1
	s_cmpk_gt_u32 s10, 0x6f
	s_mul_i32 s9, s7, 0x3800000
	v_readlane_b32 s12, v255, 3
	s_cselect_b64 s[4:5], -1, 0
	s_mul_hi_u32 s8, s7, 0x3800000
	v_readlane_b32 s13, v255, 4
	s_add_u32 s12, s12, s9
	s_addc_u32 s13, s13, s8
	s_and_b64 s[8:9], s[4:5], exec
	s_cselect_b32 s8, 0x1c00000, 0
	v_cndmask_b32_e64 v2, 0, 1, s[4:5]
	s_add_u32 s8, s12, s8
	s_addc_u32 s9, s13, 0
	s_lshl_b32 s7, s7, 1
	v_readfirstlane_b32 s12, v2
	s_or_b32 s7, s7, s12
	s_mul_hi_u32 s12, s7, 0xe00000
	s_mul_i32 s7, s7, 0xe00000
	v_readlane_b32 s13, v250, 16
	s_add_u32 s7, s13, s7
	v_readlane_b32 s13, v250, 17
	s_addc_u32 s12, s13, s12
	s_and_b64 s[4:5], s[4:5], exec
	s_cselect_b32 s4, 0xffffffc8, 0
	s_add_i32 s5, s4, s11
	s_lshl_b32 s4, s10, 10
	s_lshl_b32 s10, s5, 6
	v_or_b32_e32 v2, s10, v126
	s_and_b32 s4, s4, 0x400
	v_ashrrev_i32_e32 v3, 31, v2
	s_add_i32 s4, s4, s16
	v_lshlrev_b64 v[2:3], 13, v[2:3]
	v_lshl_add_u64 v[2:3], s[8:9], 0, v[2:3]
	s_ashr_i32 s5, s4, 31
	v_lshl_add_u64 v[2:3], s[4:5], 2, v[2:3]
	v_mov_b32_e32 v133, v187
	v_lshl_add_u64 v[2:3], v[2:3], 0, v[132:133]
	s_movk_i32 s5, 0x2000
	v_add_co_u32_e32 v6, vcc, s5, v2
	s_movk_i32 s5, 0x4000
	s_nop 0
	v_addc_co_u32_e32 v7, vcc, 0, v3, vcc
	v_add_co_u32_e32 v10, vcc, s5, v2
	s_movk_i32 s5, 0x6000
	s_nop 0
	v_addc_co_u32_e32 v11, vcc, 0, v3, vcc
	v_add_co_u32_e32 v14, vcc, s5, v2
	s_mov_b32 s5, 0x8000
	s_nop 0
	v_addc_co_u32_e32 v15, vcc, 0, v3, vcc
	v_add_co_u32_e32 v18, vcc, s5, v2
	s_mov_b32 s5, 0xa000
	s_nop 0
	v_addc_co_u32_e32 v19, vcc, 0, v3, vcc
	v_add_co_u32_e32 v22, vcc, s5, v2
	s_mov_b32 s5, 0xc000
	s_nop 0
	v_addc_co_u32_e32 v23, vcc, 0, v3, vcc
	v_add_co_u32_e32 v26, vcc, s5, v2
	global_load_dwordx4 v[98:101], v[2:3], off nt
	global_load_dwordx4 v[102:105], v[6:7], off nt
	v_addc_co_u32_e32 v27, vcc, 0, v3, vcc
	global_load_dwordx4 v[106:109], v[10:11], off nt
	global_load_dwordx4 v[110:113], v[14:15], off nt
	global_load_dwordx4 v[114:117], v[18:19], off nt
	global_load_dwordx4 v[118:121], v[22:23], off nt
	global_load_dwordx4 v[122:125], v[26:27], off nt
	s_mov_b32 s5, 0xe000
	v_add_co_u32_e32 v30, vcc, s5, v2
	s_ashr_i32 s11, s10, 31
	s_nop 0
	v_addc_co_u32_e32 v31, vcc, 0, v3, vcc
	global_load_dwordx4 v[134:137], v[30:31], off nt
	global_load_dwordx4 v[66:69], v[2:3], off offset:128 nt
	global_load_dwordx4 v[70:73], v[6:7], off offset:128 nt
	global_load_dwordx4 v[74:77], v[10:11], off offset:128 nt
	global_load_dwordx4 v[78:81], v[14:15], off offset:128 nt
	global_load_dwordx4 v[82:85], v[18:19], off offset:128 nt
	global_load_dwordx4 v[86:89], v[22:23], off offset:128 nt
	global_load_dwordx4 v[90:93], v[26:27], off offset:128 nt
	global_load_dwordx4 v[94:97], v[30:31], off offset:128 nt
	global_load_dwordx4 v[34:37], v[2:3], off offset:256 nt
	global_load_dwordx4 v[38:41], v[6:7], off offset:256 nt
	global_load_dwordx4 v[42:45], v[10:11], off offset:256 nt
	global_load_dwordx4 v[46:49], v[14:15], off offset:256 nt
	global_load_dwordx4 v[50:53], v[18:19], off offset:256 nt
	global_load_dwordx4 v[54:57], v[22:23], off offset:256 nt
	global_load_dwordx4 v[58:61], v[26:27], off offset:256 nt
	global_load_dwordx4 v[62:65], v[30:31], off offset:256 nt
	s_nop 0
	global_load_dwordx4 v[2:5], v[2:3], off offset:384 nt
	s_nop 0
	global_load_dwordx4 v[6:9], v[6:7], off offset:384 nt
	s_nop 0
	global_load_dwordx4 v[10:13], v[10:11], off offset:384 nt
	s_nop 0
	global_load_dwordx4 v[14:17], v[14:15], off offset:384 nt
	s_nop 0
	global_load_dwordx4 v[18:21], v[18:19], off offset:384 nt
	s_nop 0
	global_load_dwordx4 v[22:25], v[22:23], off offset:384 nt
	s_nop 0
	global_load_dwordx4 v[26:29], v[26:27], off offset:384 nt
	s_nop 0
	global_load_dwordx4 v[30:33], v[30:31], off offset:384 nt
	v_or_b32_e32 v133, s4, v128
	s_lshl_b64 s[4:5], s[10:11], 1
	s_add_u32 s4, s7, s4
	s_addc_u32 s5, s12, s5
	v_mov_b32_e32 v131, v187
	v_lshl_add_u64 v[142:143], s[4:5], 0, v[130:131]
	s_movk_i32 s8, 0x1c00
	v_mad_i64_i32 v[144:145], s[4:5], v133, s8, v[142:143]
	s_movk_i32 s7, 0x1000
	s_movk_i32 s9, 0x3000
	s_movk_i32 s10, 0x5000
	v_readlane_b32 s14, v255, 5
	v_readlane_b32 s15, v255, 6
	s_movk_i32 s97, 0x1000
	s_waitcnt vmcnt(30)
	v_cvt_pk_bf16_f32 v138, v98, v102
	v_add_co_u32_e32 v98, vcc, s7, v144
	s_waitcnt vmcnt(28)
	v_cvt_pk_bf16_f32 v139, v106, v110
	s_waitcnt vmcnt(26)
	v_cvt_pk_bf16_f32 v140, v114, v118
	s_waitcnt vmcnt(24)
	v_cvt_pk_bf16_f32 v141, v122, v134
	global_store_dwordx4 v[144:145], v[138:141], off nt
	s_nop 1
	v_cvt_pk_bf16_f32 v138, v99, v103
	v_cvt_pk_bf16_f32 v139, v107, v111
	v_cvt_pk_bf16_f32 v140, v115, v119
	v_cvt_pk_bf16_f32 v141, v123, v135
	v_addc_co_u32_e32 v99, vcc, 0, v145, vcc
	global_store_dwordx4 v[98:99], v[138:141], off offset:3072 nt
	v_add_co_u32_e32 v98, vcc, s9, v144
	s_nop 0
	v_cvt_pk_bf16_f32 v138, v100, v104
	v_addc_co_u32_e32 v99, vcc, 0, v145, vcc
	v_cvt_pk_bf16_f32 v139, v108, v112
	v_cvt_pk_bf16_f32 v140, v116, v120
	v_cvt_pk_bf16_f32 v141, v124, v136
	v_add_co_u32_e32 v102, vcc, s10, v144
	global_store_dwordx4 v[98:99], v[138:141], off offset:2048 nt
	v_cvt_pk_bf16_f32 v98, v101, v105
	v_cvt_pk_bf16_f32 v99, v109, v113
	v_cvt_pk_bf16_f32 v100, v117, v121
	v_cvt_pk_bf16_f32 v101, v125, v137
	v_addc_co_u32_e32 v103, vcc, 0, v145, vcc
	global_store_dwordx4 v[102:103], v[98:101], off offset:1024 nt
	s_nop 1
	v_or_b32_e32 v98, 32, v133
	v_mad_i64_i32 v[102:103], s[4:5], v98, s8, v[142:143]
	s_waitcnt vmcnt(26)
; __device__ __forceinline__ unsigned cvt_pk_bf16(float lo, float hi) { f32x2_t v = {lo, hi}; bf16x2_t b = __builtin_convertvector(v, bf16x2_t); return __builtin_bit_cast(unsigned, b); }
; __device__ __forceinline__ void conv_span128(const float* W, int ldw, int K, bf16* WT, int rowmode, int kb, int n0, int lane) {
;     const int c = lane & 7, nn = lane >> 3;
;     const float* src = W + (size_t)(kb * 64 + 8 * c) * ldw + n0 + 4 * nn;
;     f32x4 v[4][8];
; #pragma unroll
;     for (int h = 0; h < 4; ++h)
; #pragma unroll
;         for (int i = 0; i < 8; ++i) v[h][i] = __builtin_nontemporal_load((const f32x4*)(src + 32 * h + (size_t)i * ldw));
; #pragma unroll
;     for (int h = 0; h < 4; ++h) {
;         const int n = n0 + 32 * h + 4 * nn; int r = n;
;         if (rowmode == 2) r = ((n >> 7) << 8) + (n & 127);
;         else if (rowmode == 3) r = ((n >> 7) << 8) + 128 + (n & 127);
;         bf16* d0 = WT + (size_t)r * K + kb * 64 + 8 * c;
; #pragma unroll
;         for (int j = 0; j < 4; ++j) { u32x4 o; o.x = cvt_pk_bf16(v[h][0][j], v[h][1][j]); o.y = cvt_pk_bf16(v[h][2][j], v[h][3][j]); o.z = cvt_pk_bf16(v[h][4][j], v[h][5][j]); o.w = cvt_pk_bf16(v[h][6][j], v[h][7][j]);
;             *(u32x4*)(d0 + (size_t)j * K) = o; }
;     }
; }
;     ...
;         if ((cur >> 31) == 0u) { const int e = p / 448, w3 = (p / 224) & 1, q = p % 224;
;             conv_span128((w3 ? m3 : m1) + (size_t)e * D * FFE, FFE, D, mup + (size_t)e * 2 * FFE * D, 2 + w3, q / 7, (q % 7) * 1024 + wave * 128, lane); }
	v_cvt_pk_bf16_f32 v98, v66, v70
	s_waitcnt vmcnt(24)
	v_cvt_pk_bf16_f32 v99, v74, v78
	s_waitcnt vmcnt(22)
	v_cvt_pk_bf16_f32 v100, v82, v86
	s_waitcnt vmcnt(20)
	v_cvt_pk_bf16_f32 v101, v90, v94
	v_add_co_u32_e32 v66, vcc, s7, v102
	global_store_dwordx4 v[102:103], v[98:101], off nt
	s_nop 1
	v_cvt_pk_bf16_f32 v98, v67, v71
	v_cvt_pk_bf16_f32 v99, v75, v79
	v_cvt_pk_bf16_f32 v100, v83, v87
	v_cvt_pk_bf16_f32 v101, v91, v95
	v_addc_co_u32_e32 v67, vcc, 0, v103, vcc
	global_store_dwordx4 v[66:67], v[98:101], off offset:3072 nt
	v_add_co_u32_e32 v66, vcc, s9, v102
	s_nop 0
	v_cvt_pk_bf16_f32 v98, v68, v72
	v_addc_co_u32_e32 v67, vcc, 0, v103, vcc
	v_cvt_pk_bf16_f32 v99, v76, v80
	v_cvt_pk_bf16_f32 v100, v84, v88
	v_cvt_pk_bf16_f32 v101, v92, v96
	v_add_co_u32_e32 v70, vcc, s10, v102
	global_store_dwordx4 v[66:67], v[98:101], off offset:2048 nt
	v_cvt_pk_bf16_f32 v66, v69, v73
	v_cvt_pk_bf16_f32 v67, v77, v81
	v_cvt_pk_bf16_f32 v68, v85, v89
	v_cvt_pk_bf16_f32 v69, v93, v97
	v_addc_co_u32_e32 v71, vcc, 0, v103, vcc
	global_store_dwordx4 v[70:71], v[66:69], off offset:1024 nt
	s_nop 1
	v_or_b32_e32 v66, 64, v133
	v_mad_i64_i32 v[70:71], s[4:5], v66, s8, v[142:143]
	s_waitcnt vmcnt(22)
	v_cvt_pk_bf16_f32 v66, v34, v38
	s_waitcnt vmcnt(20)
	v_cvt_pk_bf16_f32 v67, v42, v46
	s_waitcnt vmcnt(18)
	v_cvt_pk_bf16_f32 v68, v50, v54
	s_waitcnt vmcnt(16)
	v_cvt_pk_bf16_f32 v69, v58, v62
	v_add_co_u32_e32 v34, vcc, s7, v70
	global_store_dwordx4 v[70:71], v[66:69], off nt
	s_nop 1
	v_cvt_pk_bf16_f32 v66, v35, v39
	v_cvt_pk_bf16_f32 v67, v43, v47
	v_cvt_pk_bf16_f32 v68, v51, v55
	v_cvt_pk_bf16_f32 v69, v59, v63
	v_addc_co_u32_e32 v35, vcc, 0, v71, vcc
	global_store_dwordx4 v[34:35], v[66:69], off offset:3072 nt
	v_add_co_u32_e32 v34, vcc, s9, v70
	s_nop 0
	v_cvt_pk_bf16_f32 v66, v36, v40
	v_addc_co_u32_e32 v35, vcc, 0, v71, vcc
	v_cvt_pk_bf16_f32 v67, v44, v48
	v_cvt_pk_bf16_f32 v68, v52, v56
	v_cvt_pk_bf16_f32 v69, v60, v64
	v_add_co_u32_e32 v38, vcc, s10, v70
	global_store_dwordx4 v[34:35], v[66:69], off offset:2048 nt
	v_cvt_pk_bf16_f32 v34, v37, v41
	v_cvt_pk_bf16_f32 v35, v45, v49
	v_cvt_pk_bf16_f32 v36, v53, v57
	v_cvt_pk_bf16_f32 v37, v61, v65
	v_addc_co_u32_e32 v39, vcc, 0, v71, vcc
	global_store_dwordx4 v[38:39], v[34:37], off offset:1024 nt
	s_nop 1
	v_or_b32_e32 v34, 0x60, v133
	v_mad_i64_i32 v[38:39], s[4:5], v34, s8, v[142:143]
	s_waitcnt vmcnt(18)
	v_cvt_pk_bf16_f32 v34, v2, v6
	s_waitcnt vmcnt(16)
	v_cvt_pk_bf16_f32 v35, v10, v14
	s_waitcnt vmcnt(14)
	v_cvt_pk_bf16_f32 v36, v18, v22
	s_waitcnt vmcnt(12)
	v_cvt_pk_bf16_f32 v37, v26, v30
	v_add_co_u32_e32 v2, vcc, s7, v38
	global_store_dwordx4 v[38:39], v[34:37], off nt
	s_mov_b64 s[4:5], 0
	s_nop 0
	v_cvt_pk_bf16_f32 v34, v3, v7
	v_cvt_pk_bf16_f32 v35, v11, v15
	v_cvt_pk_bf16_f32 v36, v19, v23
	v_cvt_pk_bf16_f32 v37, v27, v31
	v_addc_co_u32_e32 v3, vcc, 0, v39, vcc
	global_store_dwordx4 v[2:3], v[34:37], off offset:3072 nt
	v_add_co_u32_e32 v2, vcc, s9, v38
	s_nop 0
	v_cvt_pk_bf16_f32 v34, v4, v8
	v_addc_co_u32_e32 v3, vcc, 0, v39, vcc
	v_cvt_pk_bf16_f32 v35, v12, v16
	v_cvt_pk_bf16_f32 v36, v20, v24
	v_cvt_pk_bf16_f32 v37, v28, v32
	v_add_co_u32_e32 v6, vcc, 0x5000, v38
	global_store_dwordx4 v[2:3], v[34:37], off offset:2048 nt
	v_cvt_pk_bf16_f32 v2, v5, v9
	v_cvt_pk_bf16_f32 v3, v13, v17
	v_cvt_pk_bf16_f32 v4, v21, v25
	v_cvt_pk_bf16_f32 v5, v29, v33
	v_addc_co_u32_e32 v7, vcc, 0, v39, vcc
	global_store_dwordx4 v[6:7], v[2:5], off offset:1024 nt
.LBB0_281:
	s_andn2_b64 vcc, exec, s[4:5]
	s_cbranch_vccnz .LBB0_265
	s_lshr_b32 s5, s19, 5
	s_mul_hi_u32 s5, s5, 0x24924925
	s_and_b32 s10, s5, 1
	s_mul_hi_u32 s5, s6, 0x92492493
	s_lshr_b32 s5, s5, 7
	s_mulk_i32 s5, 0xe0
	s_lshr_b32 s4, s19, 6
	s_sub_i32 s8, s6, s5
	v_readlane_b32 s40, v255, 7
	s_mul_hi_u32 s4, s4, 0x24924925
	s_cmp_eq_u32 s10, 0
	v_readlane_b32 s44, v255, 11
	v_readlane_b32 s46, v255, 13
	v_readlane_b32 s45, v255, 12
	v_readlane_b32 s47, v255, 14
	s_cselect_b32 s6, s44, s46
	s_mul_hi_u32 s9, s4, 0x3800000
	s_mul_i32 s11, s4, 0x3800000
	s_movk_i32 s4, 0x60
	s_cselect_b32 s7, s45, s47
	s_cselect_b32 s12, 32, 0xa0
	s_cselect_b32 s5, 64, 0xc0
	s_cselect_b32 s4, s4, 0xe0
	s_add_u32 s6, s6, s11
	s_addc_u32 s7, s7, s9
	v_readlane_b32 s13, v250, 14
	s_add_u32 s11, s13, s11
	v_readlane_b32 s13, v250, 15
	s_addc_u32 s9, s13, s9
	s_and_b32 s13, s8, 0xff
	s_mul_i32 s13, s13, 37
	s_lshr_b32 s13, s13, 8
	s_sub_i32 s14, s8, s13
	s_bfe_u32 s14, s14, 0x70001
	s_add_i32 s14, s14, s13
	s_bfe_u32 s13, s14, 0x60002
	v_lshl_or_b32 v2, s13, 6, v126
	s_mul_i32 s14, s13, 7
	v_mul_u32_u24_e32 v186, 0x1c00, v2
	v_lshl_add_u64 v[2:3], v[186:187], 2, s[6:7]
	s_sub_i32 s6, s8, s14
	s_and_b32 s6, s6, 0xff
	s_lshl_b32 s6, s6, 10
	s_add_i32 s6, s6, s16
	s_ashr_i32 s7, s6, 31
	v_lshl_add_u64 v[2:3], s[6:7], 2, v[2:3]
	v_mov_b32_e32 v133, v187
	v_lshl_add_u64 v[70:71], v[2:3], 0, v[132:133]
	s_movk_i32 s7, 0x7000
	v_add_co_u32_e32 v78, vcc, s7, v70
	s_mov_b32 s7, 0xe000
	s_nop 0
	v_addc_co_u32_e32 v79, vcc, 0, v71, vcc
	v_add_co_u32_e32 v86, vcc, s7, v70
	s_mov_b32 s7, 0x15000
	s_nop 0
	v_addc_co_u32_e32 v87, vcc, 0, v71, vcc
	v_add_co_u32_e32 v94, vcc, s7, v70
	s_mov_b32 s7, 0x1c000
	s_nop 0
	v_addc_co_u32_e32 v95, vcc, 0, v71, vcc
	v_add_co_u32_e32 v102, vcc, s7, v70
	s_mov_b32 s7, 0x23000
	s_nop 0
	v_addc_co_u32_e32 v103, vcc, 0, v71, vcc
	v_add_co_u32_e32 v110, vcc, s7, v70
	s_mov_b32 s7, 0x2a000
	s_nop 0
	v_addc_co_u32_e32 v111, vcc, 0, v71, vcc
	v_add_co_u32_e32 v118, vcc, s7, v70
	global_load_dwordx4 v[2:5], v[70:71], off nt
	global_load_dwordx4 v[6:9], v[78:79], off nt
	v_addc_co_u32_e32 v119, vcc, 0, v71, vcc
	global_load_dwordx4 v[10:13], v[86:87], off nt
; __device__ __forceinline__ unsigned cvt_pk_bf16(float lo, float hi) { f32x2_t v = {lo, hi}; bf16x2_t b = __builtin_convertvector(v, bf16x2_t); return __builtin_bit_cast(unsigned, b); }
; __device__ __forceinline__ void conv_span128(const float* W, int ldw, int K, bf16* WT, int rowmode, int kb, int n0, int lane) {
;     const int c = lane & 7, nn = lane >> 3;
;     const float* src = W + (size_t)(kb * 64 + 8 * c) * ldw + n0 + 4 * nn;
;     f32x4 v[4][8];
; #pragma unroll
;     for (int h = 0; h < 4; ++h)
; #pragma unroll
;         for (int i = 0; i < 8; ++i) v[h][i] = __builtin_nontemporal_load((const f32x4*)(src + 32 * h + (size_t)i * ldw));
; #pragma unroll
;     for (int h = 0; h < 4; ++h) {
;         const int n = n0 + 32 * h + 4 * nn; int r = n;
;         if (rowmode == 2) r = ((n >> 7) << 8) + (n & 127);
;         else if (rowmode == 3) r = ((n >> 7) << 8) + 128 + (n & 127);
;         bf16* d0 = WT + (size_t)r * K + kb * 64 + 8 * c;
; #pragma unroll
;         for (int j = 0; j < 4; ++j) { u32x4 o; o.x = cvt_pk_bf16(v[h][0][j], v[h][1][j]); o.y = cvt_pk_bf16(v[h][2][j], v[h][3][j]); o.z = cvt_pk_bf16(v[h][4][j], v[h][5][j]); o.w = cvt_pk_bf16(v[h][6][j], v[h][7][j]);
;             *(u32x4*)(d0 + (size_t)j * K) = o; }
;     }
; }
	global_load_dwordx4 v[14:17], v[94:95], off nt
	global_load_dwordx4 v[18:21], v[102:103], off nt
	global_load_dwordx4 v[22:25], v[110:111], off nt
	global_load_dwordx4 v[26:29], v[118:119], off nt
	s_mov_b32 s7, 0x31000
	v_add_co_u32_e32 v132, vcc, s7, v70
	s_lshl_b32 s7, s13, 7
	s_nop 0
	v_addc_co_u32_e32 v133, vcc, 0, v71, vcc
	global_load_dwordx4 v[30:33], v[132:133], off nt
	global_load_dwordx4 v[34:37], v[70:71], off offset:128 nt
	global_load_dwordx4 v[38:41], v[78:79], off offset:128 nt
	global_load_dwordx4 v[42:45], v[86:87], off offset:128 nt
	global_load_dwordx4 v[46:49], v[94:95], off offset:128 nt
	global_load_dwordx4 v[50:53], v[102:103], off offset:128 nt
	global_load_dwordx4 v[54:57], v[110:111], off offset:128 nt
	global_load_dwordx4 v[58:61], v[118:119], off offset:128 nt
	global_load_dwordx4 v[62:65], v[132:133], off offset:128 nt
	global_load_dwordx4 v[66:69], v[70:71], off offset:256 nt
	s_nop 0
	global_load_dwordx4 v[70:73], v[70:71], off offset:384 nt
	s_nop 0
	global_load_dwordx4 v[74:77], v[78:79], off offset:256 nt
	s_nop 0
	global_load_dwordx4 v[78:81], v[78:79], off offset:384 nt
	s_nop 0
	global_load_dwordx4 v[82:85], v[86:87], off offset:256 nt
	s_nop 0
	global_load_dwordx4 v[86:89], v[86:87], off offset:384 nt
	s_nop 0
	global_load_dwordx4 v[90:93], v[94:95], off offset:256 nt
	s_nop 0
	global_load_dwordx4 v[94:97], v[94:95], off offset:384 nt
	s_nop 0
	global_load_dwordx4 v[98:101], v[102:103], off offset:256 nt
	s_nop 0
	global_load_dwordx4 v[102:105], v[102:103], off offset:384 nt
	s_nop 0
	global_load_dwordx4 v[106:109], v[110:111], off offset:256 nt
	s_nop 0
	global_load_dwordx4 v[110:113], v[110:111], off offset:384 nt
	s_nop 0
	global_load_dwordx4 v[114:117], v[118:119], off offset:256 nt
	s_nop 0
	global_load_dwordx4 v[118:121], v[118:119], off offset:384 nt
	s_nop 0
	global_load_dwordx4 v[122:125], v[132:133], off offset:256 nt
	s_nop 0
	global_load_dwordx4 v[132:135], v[132:133], off offset:384 nt
	s_add_u32 s8, s11, s7
	s_addc_u32 s9, s9, 0
	s_lshl_b32 s6, s6, 1
	v_lshl_or_b32 v136, s10, 7, v128
	v_or_b32_e32 v136, s6, v136
	v_mov_b32_e32 v131, v187
	v_ashrrev_i32_e32 v137, 31, v136
	v_lshl_add_u64 v[130:131], s[8:9], 0, v[130:131]
	v_lshlrev_b64 v[136:137], 12, v[136:137]
	v_lshl_add_u64 v[140:141], v[130:131], 0, v[136:137]
	s_movk_i32 s7, 0x2000
	s_movk_i32 s8, 0x3000
	v_readlane_b32 s41, v255, 8
	v_readlane_b32 s42, v255, 9
	v_readlane_b32 s43, v255, 10
	s_waitcnt vmcnt(30)
	v_cvt_pk_bf16_f32 v136, v2, v6
	v_add_co_u32_e32 v2, vcc, s7, v140
	s_waitcnt vmcnt(28)
	v_cvt_pk_bf16_f32 v137, v10, v14
	s_waitcnt vmcnt(26)
	v_cvt_pk_bf16_f32 v138, v18, v22
	s_waitcnt vmcnt(24)
	v_cvt_pk_bf16_f32 v139, v26, v30
	global_store_dwordx4 v[140:141], v[136:139], off nt
	s_nop 1
	v_cvt_pk_bf16_f32 v136, v3, v7
	v_cvt_pk_bf16_f32 v137, v11, v15
	v_cvt_pk_bf16_f32 v138, v19, v23
	v_cvt_pk_bf16_f32 v139, v27, v31
	v_addc_co_u32_e32 v3, vcc, 0, v141, vcc
	global_store_dwordx4 v[2:3], v[136:139], off offset:-4096 nt
	v_add_co_u32_e32 v6, vcc, s8, v140
	s_nop 0
	v_cvt_pk_bf16_f32 v136, v4, v8
	v_cvt_pk_bf16_f32 v137, v12, v16
	v_cvt_pk_bf16_f32 v138, v20, v24
	v_cvt_pk_bf16_f32 v139, v28, v32
	global_store_dwordx4 v[2:3], v[136:139], off nt
	v_cvt_pk_bf16_f32 v2, v5, v9
	v_cvt_pk_bf16_f32 v3, v13, v17
	v_cvt_pk_bf16_f32 v4, v21, v25
	v_cvt_pk_bf16_f32 v5, v29, v33
	v_addc_co_u32_e32 v7, vcc, 0, v141, vcc
	global_store_dwordx4 v[6:7], v[2:5], off nt
	s_nop 1
	v_or_b32_e32 v2, s12, v128
	v_or_b32_e32 v2, s6, v2
	v_ashrrev_i32_e32 v3, 31, v2
	v_lshlrev_b64 v[2:3], 12, v[2:3]
	v_lshl_add_u64 v[6:7], v[130:131], 0, v[2:3]
	s_waitcnt vmcnt(26)
	v_cvt_pk_bf16_f32 v2, v34, v38
	s_waitcnt vmcnt(24)
	v_cvt_pk_bf16_f32 v3, v42, v46
	s_waitcnt vmcnt(22)
	v_cvt_pk_bf16_f32 v4, v50, v54
	s_waitcnt vmcnt(20)
	v_cvt_pk_bf16_f32 v5, v58, v62
	v_add_co_u32_e32 v8, vcc, s7, v6
	global_store_dwordx4 v[6:7], v[2:5], off nt
	s_nop 0
	v_addc_co_u32_e32 v9, vcc, 0, v7, vcc
	v_cvt_pk_bf16_f32 v2, v35, v39
	v_cvt_pk_bf16_f32 v3, v43, v47
	v_cvt_pk_bf16_f32 v4, v51, v55
	v_cvt_pk_bf16_f32 v5, v59, v63
	global_store_dwordx4 v[8:9], v[2:5], off offset:-4096 nt
	v_add_co_u32_e32 v6, vcc, s8, v6
	s_nop 0
	v_cvt_pk_bf16_f32 v2, v36, v40
	v_cvt_pk_bf16_f32 v3, v44, v48
	v_cvt_pk_bf16_f32 v4, v52, v56
	v_cvt_pk_bf16_f32 v5, v60, v64
	global_store_dwordx4 v[8:9], v[2:5], off nt
	v_addc_co_u32_e32 v7, vcc, 0, v7, vcc
	s_nop 0
	v_cvt_pk_bf16_f32 v2, v37, v41
	v_cvt_pk_bf16_f32 v3, v45, v49
	v_cvt_pk_bf16_f32 v4, v53, v57
	v_cvt_pk_bf16_f32 v5, v61, v65
	global_store_dwordx4 v[6:7], v[2:5], off nt
	s_nop 1
	v_or_b32_e32 v2, s5, v128
	v_or_b32_e32 v2, s6, v2
	v_ashrrev_i32_e32 v3, 31, v2
	v_lshlrev_b64 v[2:3], 12, v[2:3]
	v_lshl_add_u64 v[6:7], v[130:131], 0, v[2:3]
	s_waitcnt vmcnt(21)
	v_cvt_pk_bf16_f32 v2, v66, v74
	s_waitcnt vmcnt(17)
	v_cvt_pk_bf16_f32 v3, v82, v90
	s_waitcnt vmcnt(13)
	v_cvt_pk_bf16_f32 v4, v98, v106
	s_waitcnt vmcnt(9)
	v_cvt_pk_bf16_f32 v5, v114, v122
	v_add_co_u32_e32 v8, vcc, s7, v6
	global_store_dwordx4 v[6:7], v[2:5], off nt
	s_nop 0
	v_addc_co_u32_e32 v9, vcc, 0, v7, vcc
	v_cvt_pk_bf16_f32 v2, v67, v75
	v_cvt_pk_bf16_f32 v3, v83, v91
	v_cvt_pk_bf16_f32 v4, v99, v107
	v_cvt_pk_bf16_f32 v5, v115, v123
	global_store_dwordx4 v[8:9], v[2:5], off offset:-4096 nt
	v_add_co_u32_e32 v6, vcc, s8, v6
	s_nop 0
	v_cvt_pk_bf16_f32 v2, v68, v76
	v_cvt_pk_bf16_f32 v3, v84, v92
	v_cvt_pk_bf16_f32 v4, v100, v108
	v_cvt_pk_bf16_f32 v5, v116, v124
	global_store_dwordx4 v[8:9], v[2:5], off nt
	v_addc_co_u32_e32 v7, vcc, 0, v7, vcc
	s_nop 0
	v_cvt_pk_bf16_f32 v2, v69, v77
	v_cvt_pk_bf16_f32 v3, v85, v93
	v_cvt_pk_bf16_f32 v4, v101, v109
	v_cvt_pk_bf16_f32 v5, v117, v125
	global_store_dwordx4 v[6:7], v[2:5], off nt
	s_nop 1
	v_or_b32_e32 v2, s4, v128
	v_or_b32_e32 v2, s6, v2
	v_ashrrev_i32_e32 v3, 31, v2
	v_lshlrev_b64 v[2:3], 12, v[2:3]
	v_lshl_add_u64 v[6:7], v[130:131], 0, v[2:3]
	v_cvt_pk_bf16_f32 v2, v70, v78
	v_cvt_pk_bf16_f32 v3, v86, v94
	v_cvt_pk_bf16_f32 v4, v102, v110
	s_waitcnt vmcnt(12)
	v_cvt_pk_bf16_f32 v5, v118, v132
	v_add_co_u32_e32 v8, vcc, s7, v6
	global_store_dwordx4 v[6:7], v[2:5], off nt
	s_nop 0
	v_addc_co_u32_e32 v9, vcc, 0, v7, vcc
	v_cvt_pk_bf16_f32 v2, v71, v79
	v_cvt_pk_bf16_f32 v3, v87, v95
	v_cvt_pk_bf16_f32 v4, v103, v111
	v_cvt_pk_bf16_f32 v5, v119, v133
	global_store_dwordx4 v[8:9], v[2:5], off offset:-4096 nt
	v_add_co_u32_e32 v6, vcc, 0x3000, v6
	s_nop 0
	v_cvt_pk_bf16_f32 v2, v72, v80
	v_cvt_pk_bf16_f32 v3, v88, v96
	v_cvt_pk_bf16_f32 v4, v104, v112
	v_cvt_pk_bf16_f32 v5, v120, v134
	global_store_dwordx4 v[8:9], v[2:5], off nt
	v_addc_co_u32_e32 v7, vcc, 0, v7, vcc
	s_nop 0
	v_cvt_pk_bf16_f32 v2, v73, v81
	v_cvt_pk_bf16_f32 v3, v89, v97
	v_cvt_pk_bf16_f32 v4, v105, v113
	v_cvt_pk_bf16_f32 v5, v121, v135
	global_store_dwordx4 v[6:7], v[2:5], off nt
	s_branch .LBB0_265

; __device__ __forceinline__ unsigned cvt_pk_bf16(float lo, float hi) { f32x2_t v = {lo, hi}; bf16x2_t b = __builtin_convertvector(v, bf16x2_t); return __builtin_bit_cast(unsigned, b); }
; __device__ __forceinline__ void conv_span128(const float* W, int ldw, int K, bf16* WT, int rowmode, int kb, int n0, int lane) {
;     const int c = lane & 7, nn = lane >> 3;
;     const float* src = W + (size_t)(kb * 64 + 8 * c) * ldw + n0 + 4 * nn;
;     f32x4 v[4][8];
; #pragma unroll
;     for (int h = 0; h < 4; ++h)
; #pragma unroll
;         for (int i = 0; i < 8; ++i) v[h][i] = __builtin_nontemporal_load((const f32x4*)(src + 32 * h + (size_t)i * ldw));
; #pragma unroll
;     for (int h = 0; h < 4; ++h) {
;         const int n = n0 + 32 * h + 4 * nn; int r = n;
;         if (rowmode == 2) r = ((n >> 7) << 8) + (n & 127);
;         else if (rowmode == 3) r = ((n >> 7) << 8) + 128 + (n & 127);
;         bf16* d0 = WT + (size_t)r * K + kb * 64 + 8 * c;
; #pragma unroll
;         for (int j = 0; j < 4; ++j) { u32x4 o; o.x = cvt_pk_bf16(v[h][0][j], v[h][1][j]); o.y = cvt_pk_bf16(v[h][2][j], v[h][3][j]); o.z = cvt_pk_bf16(v[h][4][j], v[h][5][j]); o.w = cvt_pk_bf16(v[h][6][j], v[h][7][j]);
;             *(u32x4*)(d0 + (size_t)j * K) = o; }
;     }
; }
;     ...
;         else { const int e = p / 224, q = p % 224, kb = q >> 1, h = kb / 56;
;             conv_span128(m2 + (size_t)e * FFE * D + (size_t)h * (FFE / 2) * D, 2048, FFE / 2, mdn + (size_t)(e * 2 + h) * D * (FFE / 2), 0, kb - 56 * h, (q & 1) * 1024 + wave * 128, lane); }
.LBB0_527:
	s_or_b64 exec, exec, s[6:7]
	s_and_b32 s8, s20, 0x7fffffff
	s_mov_b64 s[6:7], -1
	s_cmp_lt_i32 s20, 0
	v_lshlrev_b32_e32 v132, 2, v128
	v_lshlrev_b32_e32 v130, 1, v126
	s_cbranch_scc0 .LBB0_529
	s_lshr_b32 s6, s8, 5
	s_mul_hi_u32 s9, s6, 0x24924925
	s_mul_i32 s6, s9, 0xe0
	s_sub_i32 s12, s8, s6
	s_lshr_b32 s13, s12, 1
	s_cmpk_gt_u32 s12, 0x6f
	s_mul_i32 s11, s9, 0x3800000
	v_readlane_b32 s40, v255, 3
	s_cselect_b64 s[6:7], -1, 0
	s_mul_hi_u32 s10, s9, 0x3800000
	v_readlane_b32 s41, v255, 4
	s_add_u32 s14, s40, s11
	s_addc_u32 s15, s41, s10
	s_and_b64 s[10:11], s[6:7], exec
	s_cselect_b32 s10, 0x1c00000, 0
	v_cndmask_b32_e64 v2, 0, 1, s[6:7]
	s_add_u32 s10, s14, s10
	s_addc_u32 s11, s15, 0
	s_lshl_b32 s9, s9, 1
	v_readfirstlane_b32 s14, v2
	s_or_b32 s9, s9, s14
	s_mul_hi_u32 s14, s9, 0xe00000
	s_mul_i32 s9, s9, 0xe00000
	v_readlane_b32 s15, v250, 16
	s_add_u32 s9, s15, s9
	v_readlane_b32 s15, v250, 17
	s_addc_u32 s14, s15, s14
	s_and_b64 s[6:7], s[6:7], exec
	s_cselect_b32 s6, 0xffffffc8, 0
	s_add_i32 s7, s6, s13
	s_lshl_b32 s6, s12, 10
	s_lshl_b32 s12, s7, 6
	v_or_b32_e32 v2, s12, v126
	s_and_b32 s6, s6, 0x400
	v_ashrrev_i32_e32 v3, 31, v2
	s_add_i32 s6, s6, s18
	v_lshlrev_b64 v[2:3], 13, v[2:3]
	v_lshl_add_u64 v[2:3], s[10:11], 0, v[2:3]
	s_ashr_i32 s7, s6, 31
	v_lshl_add_u64 v[2:3], s[6:7], 2, v[2:3]
	v_mov_b32_e32 v133, v187
	v_lshl_add_u64 v[2:3], v[2:3], 0, v[132:133]
	s_movk_i32 s7, 0x2000
	v_add_co_u32_e32 v6, vcc, s7, v2
	s_movk_i32 s7, 0x4000
	s_nop 0
	v_addc_co_u32_e32 v7, vcc, 0, v3, vcc
	v_add_co_u32_e32 v10, vcc, s7, v2
	s_movk_i32 s7, 0x6000
	s_nop 0
	v_addc_co_u32_e32 v11, vcc, 0, v3, vcc
	v_add_co_u32_e32 v14, vcc, s7, v2
	s_mov_b32 s7, 0x8000
	s_nop 0
	v_addc_co_u32_e32 v15, vcc, 0, v3, vcc
	v_add_co_u32_e32 v18, vcc, s7, v2
	s_mov_b32 s7, 0xa000
	s_nop 0
	v_addc_co_u32_e32 v19, vcc, 0, v3, vcc
	v_add_co_u32_e32 v22, vcc, s7, v2
	s_mov_b32 s7, 0xc000
	s_nop 0
	v_addc_co_u32_e32 v23, vcc, 0, v3, vcc
	v_add_co_u32_e32 v26, vcc, s7, v2
	global_load_dwordx4 v[98:101], v[2:3], off nt
	global_load_dwordx4 v[102:105], v[6:7], off nt
	v_addc_co_u32_e32 v27, vcc, 0, v3, vcc
	global_load_dwordx4 v[106:109], v[10:11], off nt
	global_load_dwordx4 v[110:113], v[14:15], off nt
	global_load_dwordx4 v[114:117], v[18:19], off nt
	global_load_dwordx4 v[118:121], v[22:23], off nt
	global_load_dwordx4 v[122:125], v[26:27], off nt
	s_mov_b32 s7, 0xe000
	v_add_co_u32_e32 v30, vcc, s7, v2
	s_ashr_i32 s13, s12, 31
	s_nop 0
	v_addc_co_u32_e32 v31, vcc, 0, v3, vcc
	global_load_dwordx4 v[134:137], v[30:31], off nt
	global_load_dwordx4 v[66:69], v[2:3], off offset:128 nt
	global_load_dwordx4 v[70:73], v[6:7], off offset:128 nt
	global_load_dwordx4 v[74:77], v[10:11], off offset:128 nt
	global_load_dwordx4 v[78:81], v[14:15], off offset:128 nt
	global_load_dwordx4 v[82:85], v[18:19], off offset:128 nt
	global_load_dwordx4 v[86:89], v[22:23], off offset:128 nt
	global_load_dwordx4 v[90:93], v[26:27], off offset:128 nt
	global_load_dwordx4 v[94:97], v[30:31], off offset:128 nt
	global_load_dwordx4 v[34:37], v[2:3], off offset:256 nt
	global_load_dwordx4 v[38:41], v[6:7], off offset:256 nt
	global_load_dwordx4 v[42:45], v[10:11], off offset:256 nt
	global_load_dwordx4 v[46:49], v[14:15], off offset:256 nt
	global_load_dwordx4 v[50:53], v[18:19], off offset:256 nt
	global_load_dwordx4 v[54:57], v[22:23], off offset:256 nt
	global_load_dwordx4 v[58:61], v[26:27], off offset:256 nt
	global_load_dwordx4 v[62:65], v[30:31], off offset:256 nt
	s_nop 0
	global_load_dwordx4 v[2:5], v[2:3], off offset:384 nt
	s_nop 0
	global_load_dwordx4 v[6:9], v[6:7], off offset:384 nt
	s_nop 0
	global_load_dwordx4 v[10:13], v[10:11], off offset:384 nt
	s_nop 0
	global_load_dwordx4 v[14:17], v[14:15], off offset:384 nt
	s_nop 0
	global_load_dwordx4 v[18:21], v[18:19], off offset:384 nt
	s_nop 0
	global_load_dwordx4 v[22:25], v[22:23], off offset:384 nt
	s_nop 0
	global_load_dwordx4 v[26:29], v[26:27], off offset:384 nt
	s_nop 0
	global_load_dwordx4 v[30:33], v[30:31], off offset:384 nt
	v_or_b32_e32 v129, s6, v128
	s_lshl_b64 s[6:7], s[12:13], 1
	s_add_u32 s6, s9, s6
	s_addc_u32 s7, s14, s7
	v_mov_b32_e32 v131, v187
	v_lshl_add_u64 v[142:143], s[6:7], 0, v[130:131]
	s_movk_i32 s10, 0x1c00
	v_mad_i64_i32 v[144:145], s[6:7], v129, s10, v[142:143]
	s_movk_i32 s9, 0x1000
	s_movk_i32 s11, 0x3000
	s_movk_i32 s12, 0x5000
	v_readlane_b32 s42, v255, 5
	v_readlane_b32 s43, v255, 6
	s_movk_i32 s97, 0x1000
	s_waitcnt vmcnt(30)
	v_cvt_pk_bf16_f32 v138, v98, v102
	v_add_co_u32_e32 v98, vcc, s9, v144
	s_waitcnt vmcnt(28)
	v_cvt_pk_bf16_f32 v139, v106, v110
	s_waitcnt vmcnt(26)
	v_cvt_pk_bf16_f32 v140, v114, v118
	s_waitcnt vmcnt(24)
	v_cvt_pk_bf16_f32 v141, v122, v134
	global_store_dwordx4 v[144:145], v[138:141], off nt
	s_nop 1
	v_cvt_pk_bf16_f32 v138, v99, v103
	v_cvt_pk_bf16_f32 v139, v107, v111
	v_cvt_pk_bf16_f32 v140, v115, v119
	v_cvt_pk_bf16_f32 v141, v123, v135
	v_addc_co_u32_e32 v99, vcc, 0, v145, vcc
	global_store_dwordx4 v[98:99], v[138:141], off offset:3072 nt
	v_add_co_u32_e32 v98, vcc, s11, v144
	s_nop 0
	v_cvt_pk_bf16_f32 v138, v100, v104
	v_addc_co_u32_e32 v99, vcc, 0, v145, vcc
	v_cvt_pk_bf16_f32 v139, v108, v112
	v_cvt_pk_bf16_f32 v140, v116, v120
	v_cvt_pk_bf16_f32 v141, v124, v136
	v_add_co_u32_e32 v102, vcc, s12, v144
	global_store_dwordx4 v[98:99], v[138:141], off offset:2048 nt
	v_cvt_pk_bf16_f32 v98, v101, v105
	v_cvt_pk_bf16_f32 v99, v109, v113
	v_cvt_pk_bf16_f32 v100, v117, v121
	v_cvt_pk_bf16_f32 v101, v125, v137
	v_addc_co_u32_e32 v103, vcc, 0, v145, vcc
	global_store_dwordx4 v[102:103], v[98:101], off offset:1024 nt
	s_nop 1
	v_or_b32_e32 v98, 32, v129
	v_mad_i64_i32 v[102:103], s[6:7], v98, s10, v[142:143]
	s_waitcnt vmcnt(26)
; __device__ __forceinline__ unsigned cvt_pk_bf16(float lo, float hi) { f32x2_t v = {lo, hi}; bf16x2_t b = __builtin_convertvector(v, bf16x2_t); return __builtin_bit_cast(unsigned, b); }
; __device__ __forceinline__ void conv_span128(const float* W, int ldw, int K, bf16* WT, int rowmode, int kb, int n0, int lane) {
;     const int c = lane & 7, nn = lane >> 3;
;     const float* src = W + (size_t)(kb * 64 + 8 * c) * ldw + n0 + 4 * nn;
;     f32x4 v[4][8];
; #pragma unroll
;     for (int h = 0; h < 4; ++h)
; #pragma unroll
;         for (int i = 0; i < 8; ++i) v[h][i] = __builtin_nontemporal_load((const f32x4*)(src + 32 * h + (size_t)i * ldw));
; #pragma unroll
;     for (int h = 0; h < 4; ++h) {
;         const int n = n0 + 32 * h + 4 * nn; int r = n;
;         if (rowmode == 2) r = ((n >> 7) << 8) + (n & 127);
;         else if (rowmode == 3) r = ((n >> 7) << 8) + 128 + (n & 127);
;         bf16* d0 = WT + (size_t)r * K + kb * 64 + 8 * c;
; #pragma unroll
;         for (int j = 0; j < 4; ++j) { u32x4 o; o.x = cvt_pk_bf16(v[h][0][j], v[h][1][j]); o.y = cvt_pk_bf16(v[h][2][j], v[h][3][j]); o.z = cvt_pk_bf16(v[h][4][j], v[h][5][j]); o.w = cvt_pk_bf16(v[h][6][j], v[h][7][j]);
;             *(u32x4*)(d0 + (size_t)j * K) = o; }
;     }
; }
;     ...
;         if ((cur >> 31) == 0u) { const int e = p / 448, w3 = (p / 224) & 1, q = p % 224;
;             conv_span128((w3 ? m3 : m1) + (size_t)e * D * FFE, FFE, D, mup + (size_t)e * 2 * FFE * D, 2 + w3, q / 7, (q % 7) * 1024 + wave * 128, lane); }
	v_cvt_pk_bf16_f32 v98, v66, v70
	s_waitcnt vmcnt(24)
	v_cvt_pk_bf16_f32 v99, v74, v78
	s_waitcnt vmcnt(22)
	v_cvt_pk_bf16_f32 v100, v82, v86
	s_waitcnt vmcnt(20)
	v_cvt_pk_bf16_f32 v101, v90, v94
	v_add_co_u32_e32 v66, vcc, s9, v102
	global_store_dwordx4 v[102:103], v[98:101], off nt
	s_nop 1
	v_cvt_pk_bf16_f32 v98, v67, v71
	v_cvt_pk_bf16_f32 v99, v75, v79
	v_cvt_pk_bf16_f32 v100, v83, v87
	v_cvt_pk_bf16_f32 v101, v91, v95
	v_addc_co_u32_e32 v67, vcc, 0, v103, vcc
	global_store_dwordx4 v[66:67], v[98:101], off offset:3072 nt
	v_add_co_u32_e32 v66, vcc, s11, v102
	s_nop 0
	v_cvt_pk_bf16_f32 v98, v68, v72
	v_addc_co_u32_e32 v67, vcc, 0, v103, vcc
	v_cvt_pk_bf16_f32 v99, v76, v80
	v_cvt_pk_bf16_f32 v100, v84, v88
	v_cvt_pk_bf16_f32 v101, v92, v96
	v_add_co_u32_e32 v70, vcc, s12, v102
	global_store_dwordx4 v[66:67], v[98:101], off offset:2048 nt
	v_cvt_pk_bf16_f32 v66, v69, v73
	v_cvt_pk_bf16_f32 v67, v77, v81
	v_cvt_pk_bf16_f32 v68, v85, v89
	v_cvt_pk_bf16_f32 v69, v93, v97
	v_addc_co_u32_e32 v71, vcc, 0, v103, vcc
	global_store_dwordx4 v[70:71], v[66:69], off offset:1024 nt
	s_nop 1
	v_or_b32_e32 v66, 64, v129
	v_mad_i64_i32 v[70:71], s[6:7], v66, s10, v[142:143]
	s_waitcnt vmcnt(22)
	v_cvt_pk_bf16_f32 v66, v34, v38
	s_waitcnt vmcnt(20)
	v_cvt_pk_bf16_f32 v67, v42, v46
	s_waitcnt vmcnt(18)
	v_cvt_pk_bf16_f32 v68, v50, v54
	s_waitcnt vmcnt(16)
	v_cvt_pk_bf16_f32 v69, v58, v62
	v_add_co_u32_e32 v34, vcc, s9, v70
	global_store_dwordx4 v[70:71], v[66:69], off nt
	s_nop 1
	v_cvt_pk_bf16_f32 v66, v35, v39
	v_cvt_pk_bf16_f32 v67, v43, v47
	v_cvt_pk_bf16_f32 v68, v51, v55
	v_cvt_pk_bf16_f32 v69, v59, v63
	v_addc_co_u32_e32 v35, vcc, 0, v71, vcc
	global_store_dwordx4 v[34:35], v[66:69], off offset:3072 nt
	v_add_co_u32_e32 v34, vcc, s11, v70
	s_nop 0
	v_cvt_pk_bf16_f32 v66, v36, v40
	v_addc_co_u32_e32 v35, vcc, 0, v71, vcc
	v_cvt_pk_bf16_f32 v67, v44, v48
	v_cvt_pk_bf16_f32 v68, v52, v56
	v_cvt_pk_bf16_f32 v69, v60, v64
	v_add_co_u32_e32 v38, vcc, s12, v70
	global_store_dwordx4 v[34:35], v[66:69], off offset:2048 nt
	v_cvt_pk_bf16_f32 v34, v37, v41
	v_cvt_pk_bf16_f32 v35, v45, v49
	v_cvt_pk_bf16_f32 v36, v53, v57
	v_cvt_pk_bf16_f32 v37, v61, v65
	v_addc_co_u32_e32 v39, vcc, 0, v71, vcc
	global_store_dwordx4 v[38:39], v[34:37], off offset:1024 nt
	s_nop 1
	v_or_b32_e32 v34, 0x60, v129
	v_mad_i64_i32 v[38:39], s[6:7], v34, s10, v[142:143]
	s_waitcnt vmcnt(18)
	v_cvt_pk_bf16_f32 v34, v2, v6
	s_waitcnt vmcnt(16)
	v_cvt_pk_bf16_f32 v35, v10, v14
	s_waitcnt vmcnt(14)
	v_cvt_pk_bf16_f32 v36, v18, v22
	s_waitcnt vmcnt(12)
	v_cvt_pk_bf16_f32 v37, v26, v30
	v_add_co_u32_e32 v2, vcc, s9, v38
	global_store_dwordx4 v[38:39], v[34:37], off nt
	s_mov_b64 s[6:7], 0
	s_nop 0
	v_cvt_pk_bf16_f32 v34, v3, v7
	v_cvt_pk_bf16_f32 v35, v11, v15
	v_cvt_pk_bf16_f32 v36, v19, v23
	v_cvt_pk_bf16_f32 v37, v27, v31
	v_addc_co_u32_e32 v3, vcc, 0, v39, vcc
	global_store_dwordx4 v[2:3], v[34:37], off offset:3072 nt
	v_add_co_u32_e32 v2, vcc, s11, v38
	s_nop 0
	v_cvt_pk_bf16_f32 v34, v4, v8
	v_addc_co_u32_e32 v3, vcc, 0, v39, vcc
	v_cvt_pk_bf16_f32 v35, v12, v16
	v_cvt_pk_bf16_f32 v36, v20, v24
	v_cvt_pk_bf16_f32 v37, v28, v32
	v_add_co_u32_e32 v6, vcc, 0x5000, v38
	global_store_dwordx4 v[2:3], v[34:37], off offset:2048 nt
	v_cvt_pk_bf16_f32 v2, v5, v9
	v_cvt_pk_bf16_f32 v3, v13, v17
	v_cvt_pk_bf16_f32 v4, v21, v25
	v_cvt_pk_bf16_f32 v5, v29, v33
	v_addc_co_u32_e32 v7, vcc, 0, v39, vcc
	global_store_dwordx4 v[6:7], v[2:5], off offset:1024 nt
.LBB0_529:
	s_andn2_b64 vcc, exec, s[6:7]
	s_cbranch_vccnz .LBB0_511
	s_lshr_b32 s7, s20, 5
	s_mul_hi_u32 s7, s7, 0x24924925
	s_and_b32 s12, s7, 1
	s_mul_hi_u32 s7, s8, 0x92492493
	s_lshr_b32 s7, s7, 7
	s_mulk_i32 s7, 0xe0
	s_lshr_b32 s6, s20, 6
	s_sub_i32 s10, s8, s7
	v_readlane_b32 s40, v255, 7
	s_mul_hi_u32 s6, s6, 0x24924925
	s_cmp_eq_u32 s12, 0
	v_readlane_b32 s44, v255, 11
	v_readlane_b32 s46, v255, 13
	v_readlane_b32 s45, v255, 12
	v_readlane_b32 s47, v255, 14
	s_cselect_b32 s8, s44, s46
	s_mul_hi_u32 s11, s6, 0x3800000
	s_mul_i32 s13, s6, 0x3800000
	s_movk_i32 s6, 0x60
	s_cselect_b32 s9, s45, s47
	s_cselect_b32 s14, 32, 0xa0
	s_cselect_b32 s7, 64, 0xc0
	s_cselect_b32 s6, s6, 0xe0
	s_add_u32 s8, s8, s13
	s_addc_u32 s9, s9, s11
	v_readlane_b32 s15, v250, 14
	s_add_u32 s13, s15, s13
	v_readlane_b32 s15, v250, 15
	s_addc_u32 s11, s15, s11
	s_and_b32 s15, s10, 0xff
	s_mul_i32 s15, s15, 37
	s_lshr_b32 s15, s15, 8
	s_sub_i32 s16, s10, s15
	s_bfe_u32 s16, s16, 0x70001
	s_add_i32 s16, s16, s15
	s_bfe_u32 s15, s16, 0x60002
	v_lshl_or_b32 v2, s15, 6, v126
	s_mul_i32 s16, s15, 7
	v_mul_u32_u24_e32 v186, 0x1c00, v2
	v_lshl_add_u64 v[2:3], v[186:187], 2, s[8:9]
	s_sub_i32 s8, s10, s16
	s_and_b32 s8, s8, 0xff
	s_lshl_b32 s8, s8, 10
	s_add_i32 s8, s8, s18
	s_ashr_i32 s9, s8, 31
	v_lshl_add_u64 v[2:3], s[8:9], 2, v[2:3]
	v_mov_b32_e32 v133, v187
	v_lshl_add_u64 v[70:71], v[2:3], 0, v[132:133]
	s_movk_i32 s9, 0x7000
	v_add_co_u32_e32 v78, vcc, s9, v70
	s_mov_b32 s9, 0xe000
	s_nop 0
	v_addc_co_u32_e32 v79, vcc, 0, v71, vcc
	v_add_co_u32_e32 v86, vcc, s9, v70
	s_mov_b32 s9, 0x15000
	s_nop 0
	v_addc_co_u32_e32 v87, vcc, 0, v71, vcc
	v_add_co_u32_e32 v94, vcc, s9, v70
	s_mov_b32 s9, 0x1c000
	s_nop 0
	v_addc_co_u32_e32 v95, vcc, 0, v71, vcc
	v_add_co_u32_e32 v102, vcc, s9, v70
	s_mov_b32 s9, 0x23000
	s_nop 0
	v_addc_co_u32_e32 v103, vcc, 0, v71, vcc
	v_add_co_u32_e32 v110, vcc, s9, v70
	s_mov_b32 s9, 0x2a000
	s_nop 0
	v_addc_co_u32_e32 v111, vcc, 0, v71, vcc
	v_add_co_u32_e32 v118, vcc, s9, v70
	global_load_dwordx4 v[2:5], v[70:71], off nt
	global_load_dwordx4 v[6:9], v[78:79], off nt
	v_addc_co_u32_e32 v119, vcc, 0, v71, vcc
	global_load_dwordx4 v[10:13], v[86:87], off nt
; __device__ __forceinline__ unsigned cvt_pk_bf16(float lo, float hi) { f32x2_t v = {lo, hi}; bf16x2_t b = __builtin_convertvector(v, bf16x2_t); return __builtin_bit_cast(unsigned, b); }
; __device__ __forceinline__ void conv_span128(const float* W, int ldw, int K, bf16* WT, int rowmode, int kb, int n0, int lane) {
;     const int c = lane & 7, nn = lane >> 3;
;     const float* src = W + (size_t)(kb * 64 + 8 * c) * ldw + n0 + 4 * nn;
;     f32x4 v[4][8];
; #pragma unroll
;     for (int h = 0; h < 4; ++h)
; #pragma unroll
;         for (int i = 0; i < 8; ++i) v[h][i] = __builtin_nontemporal_load((const f32x4*)(src + 32 * h + (size_t)i * ldw));
; #pragma unroll
;     for (int h = 0; h < 4; ++h) {
;         const int n = n0 + 32 * h + 4 * nn; int r = n;
;         if (rowmode == 2) r = ((n >> 7) << 8) + (n & 127);
;         else if (rowmode == 3) r = ((n >> 7) << 8) + 128 + (n & 127);
;         bf16* d0 = WT + (size_t)r * K + kb * 64 + 8 * c;
; #pragma unroll
;         for (int j = 0; j < 4; ++j) { u32x4 o; o.x = cvt_pk_bf16(v[h][0][j], v[h][1][j]); o.y = cvt_pk_bf16(v[h][2][j], v[h][3][j]); o.z = cvt_pk_bf16(v[h][4][j], v[h][5][j]); o.w = cvt_pk_bf16(v[h][6][j], v[h][7][j]);
;             *(u32x4*)(d0 + (size_t)j * K) = o; }
;     }
; }
	global_load_dwordx4 v[14:17], v[94:95], off nt
	global_load_dwordx4 v[18:21], v[102:103], off nt
	global_load_dwordx4 v[22:25], v[110:111], off nt
	global_load_dwordx4 v[26:29], v[118:119], off nt
	s_mov_b32 s9, 0x31000
	v_add_co_u32_e32 v132, vcc, s9, v70
	s_lshl_b32 s9, s15, 7
	s_nop 0
	v_addc_co_u32_e32 v133, vcc, 0, v71, vcc
	global_load_dwordx4 v[30:33], v[132:133], off nt
	global_load_dwordx4 v[34:37], v[70:71], off offset:128 nt
	global_load_dwordx4 v[38:41], v[78:79], off offset:128 nt
	global_load_dwordx4 v[42:45], v[86:87], off offset:128 nt
	global_load_dwordx4 v[46:49], v[94:95], off offset:128 nt
	global_load_dwordx4 v[50:53], v[102:103], off offset:128 nt
	global_load_dwordx4 v[54:57], v[110:111], off offset:128 nt
	global_load_dwordx4 v[58:61], v[118:119], off offset:128 nt
	global_load_dwordx4 v[62:65], v[132:133], off offset:128 nt
	global_load_dwordx4 v[66:69], v[70:71], off offset:256 nt
	s_nop 0
	global_load_dwordx4 v[70:73], v[70:71], off offset:384 nt
	s_nop 0
	global_load_dwordx4 v[74:77], v[78:79], off offset:256 nt
	s_nop 0
	global_load_dwordx4 v[78:81], v[78:79], off offset:384 nt
	s_nop 0
	global_load_dwordx4 v[82:85], v[86:87], off offset:256 nt
	s_nop 0
	global_load_dwordx4 v[86:89], v[86:87], off offset:384 nt
	s_nop 0
	global_load_dwordx4 v[90:93], v[94:95], off offset:256 nt
	s_nop 0
	global_load_dwordx4 v[94:97], v[94:95], off offset:384 nt
	s_nop 0
	global_load_dwordx4 v[98:101], v[102:103], off offset:256 nt
	s_nop 0
	global_load_dwordx4 v[102:105], v[102:103], off offset:384 nt
	s_nop 0
	global_load_dwordx4 v[106:109], v[110:111], off offset:256 nt
	s_nop 0
	global_load_dwordx4 v[110:113], v[110:111], off offset:384 nt
	s_nop 0
	global_load_dwordx4 v[114:117], v[118:119], off offset:256 nt
	s_nop 0
	global_load_dwordx4 v[118:121], v[118:119], off offset:384 nt
	s_nop 0
	global_load_dwordx4 v[122:125], v[132:133], off offset:256 nt
	s_nop 0
	global_load_dwordx4 v[132:135], v[132:133], off offset:384 nt
	s_add_u32 s10, s13, s9
	s_addc_u32 s11, s11, 0
	s_lshl_b32 s8, s8, 1
	v_lshl_or_b32 v129, s12, 7, v128
	v_or_b32_e32 v136, s8, v129
	v_mov_b32_e32 v131, v187
	v_ashrrev_i32_e32 v137, 31, v136
	v_lshl_add_u64 v[130:131], s[10:11], 0, v[130:131]
	v_lshlrev_b64 v[136:137], 12, v[136:137]
	v_lshl_add_u64 v[140:141], v[130:131], 0, v[136:137]
	s_movk_i32 s9, 0x2000
	s_movk_i32 s10, 0x3000
	v_readlane_b32 s41, v255, 8
	v_readlane_b32 s42, v255, 9
	v_readlane_b32 s43, v255, 10
	s_waitcnt vmcnt(30)
	v_cvt_pk_bf16_f32 v136, v2, v6
	v_add_co_u32_e32 v2, vcc, s9, v140
	s_waitcnt vmcnt(28)
	v_cvt_pk_bf16_f32 v137, v10, v14
	s_waitcnt vmcnt(26)
	v_cvt_pk_bf16_f32 v138, v18, v22
	s_waitcnt vmcnt(24)
	v_cvt_pk_bf16_f32 v139, v26, v30
	global_store_dwordx4 v[140:141], v[136:139], off nt
	s_nop 1
	v_cvt_pk_bf16_f32 v136, v3, v7
	v_cvt_pk_bf16_f32 v137, v11, v15
	v_cvt_pk_bf16_f32 v138, v19, v23
	v_cvt_pk_bf16_f32 v139, v27, v31
	v_addc_co_u32_e32 v3, vcc, 0, v141, vcc
	global_store_dwordx4 v[2:3], v[136:139], off offset:-4096 nt
	v_add_co_u32_e32 v6, vcc, s10, v140
	s_nop 0
	v_cvt_pk_bf16_f32 v136, v4, v8
	v_cvt_pk_bf16_f32 v137, v12, v16
	v_cvt_pk_bf16_f32 v138, v20, v24
	v_cvt_pk_bf16_f32 v139, v28, v32
	global_store_dwordx4 v[2:3], v[136:139], off nt
	v_cvt_pk_bf16_f32 v2, v5, v9
	v_cvt_pk_bf16_f32 v3, v13, v17
	v_cvt_pk_bf16_f32 v4, v21, v25
	v_cvt_pk_bf16_f32 v5, v29, v33
	v_addc_co_u32_e32 v7, vcc, 0, v141, vcc
	global_store_dwordx4 v[6:7], v[2:5], off nt
	s_nop 1
	v_or_b32_e32 v2, s14, v128
	v_or_b32_e32 v2, s8, v2
	v_ashrrev_i32_e32 v3, 31, v2
	v_lshlrev_b64 v[2:3], 12, v[2:3]
	v_lshl_add_u64 v[6:7], v[130:131], 0, v[2:3]
	s_waitcnt vmcnt(26)
	v_cvt_pk_bf16_f32 v2, v34, v38
	s_waitcnt vmcnt(24)
	v_cvt_pk_bf16_f32 v3, v42, v46
	s_waitcnt vmcnt(22)
	v_cvt_pk_bf16_f32 v4, v50, v54
	s_waitcnt vmcnt(20)
	v_cvt_pk_bf16_f32 v5, v58, v62
	v_add_co_u32_e32 v8, vcc, s9, v6
	global_store_dwordx4 v[6:7], v[2:5], off nt
	s_nop 0
	v_addc_co_u32_e32 v9, vcc, 0, v7, vcc
	v_cvt_pk_bf16_f32 v2, v35, v39
	v_cvt_pk_bf16_f32 v3, v43, v47
	v_cvt_pk_bf16_f32 v4, v51, v55
	v_cvt_pk_bf16_f32 v5, v59, v63
	global_store_dwordx4 v[8:9], v[2:5], off offset:-4096 nt
	v_add_co_u32_e32 v6, vcc, s10, v6
	s_nop 0
	v_cvt_pk_bf16_f32 v2, v36, v40
	v_cvt_pk_bf16_f32 v3, v44, v48
	v_cvt_pk_bf16_f32 v4, v52, v56
	v_cvt_pk_bf16_f32 v5, v60, v64
	global_store_dwordx4 v[8:9], v[2:5], off nt
	v_addc_co_u32_e32 v7, vcc, 0, v7, vcc
	s_nop 0
	v_cvt_pk_bf16_f32 v2, v37, v41
	v_cvt_pk_bf16_f32 v3, v45, v49
	v_cvt_pk_bf16_f32 v4, v53, v57
	v_cvt_pk_bf16_f32 v5, v61, v65
	global_store_dwordx4 v[6:7], v[2:5], off nt
	s_nop 1
	v_or_b32_e32 v2, s7, v128
	v_or_b32_e32 v2, s8, v2
	v_ashrrev_i32_e32 v3, 31, v2
	v_lshlrev_b64 v[2:3], 12, v[2:3]
	v_lshl_add_u64 v[6:7], v[130:131], 0, v[2:3]
	s_waitcnt vmcnt(21)
	v_cvt_pk_bf16_f32 v2, v66, v74
	s_waitcnt vmcnt(17)
	v_cvt_pk_bf16_f32 v3, v82, v90
	s_waitcnt vmcnt(13)
	v_cvt_pk_bf16_f32 v4, v98, v106
	s_waitcnt vmcnt(9)
	v_cvt_pk_bf16_f32 v5, v114, v122
	v_add_co_u32_e32 v8, vcc, s9, v6
	global_store_dwordx4 v[6:7], v[2:5], off nt
	s_nop 0
	v_addc_co_u32_e32 v9, vcc, 0, v7, vcc
	v_cvt_pk_bf16_f32 v2, v67, v75
	v_cvt_pk_bf16_f32 v3, v83, v91
	v_cvt_pk_bf16_f32 v4, v99, v107
	v_cvt_pk_bf16_f32 v5, v115, v123
	global_store_dwordx4 v[8:9], v[2:5], off offset:-4096 nt
	v_add_co_u32_e32 v6, vcc, s10, v6
	s_nop 0
	v_cvt_pk_bf16_f32 v2, v68, v76
	v_cvt_pk_bf16_f32 v3, v84, v92
	v_cvt_pk_bf16_f32 v4, v100, v108
	v_cvt_pk_bf16_f32 v5, v116, v124
	global_store_dwordx4 v[8:9], v[2:5], off nt
	v_addc_co_u32_e32 v7, vcc, 0, v7, vcc
	s_nop 0
	v_cvt_pk_bf16_f32 v2, v69, v77
	v_cvt_pk_bf16_f32 v3, v85, v93
	v_cvt_pk_bf16_f32 v4, v101, v109
	v_cvt_pk_bf16_f32 v5, v117, v125
	global_store_dwordx4 v[6:7], v[2:5], off nt
	s_nop 1
	v_or_b32_e32 v2, s6, v128
	v_or_b32_e32 v2, s8, v2
	v_ashrrev_i32_e32 v3, 31, v2
	v_lshlrev_b64 v[2:3], 12, v[2:3]
	v_lshl_add_u64 v[6:7], v[130:131], 0, v[2:3]
	v_cvt_pk_bf16_f32 v2, v70, v78
	v_cvt_pk_bf16_f32 v3, v86, v94
	v_cvt_pk_bf16_f32 v4, v102, v110
	s_waitcnt vmcnt(12)
	v_cvt_pk_bf16_f32 v5, v118, v132
	v_add_co_u32_e32 v8, vcc, s9, v6
	global_store_dwordx4 v[6:7], v[2:5], off nt
	s_nop 0
	v_addc_co_u32_e32 v9, vcc, 0, v7, vcc
	v_cvt_pk_bf16_f32 v2, v71, v79
	v_cvt_pk_bf16_f32 v3, v87, v95
	v_cvt_pk_bf16_f32 v4, v103, v111
	v_cvt_pk_bf16_f32 v5, v119, v133
	global_store_dwordx4 v[8:9], v[2:5], off offset:-4096 nt
	v_add_co_u32_e32 v6, vcc, 0x3000, v6
	s_nop 0
	v_cvt_pk_bf16_f32 v2, v72, v80
	v_cvt_pk_bf16_f32 v3, v88, v96
	v_cvt_pk_bf16_f32 v4, v104, v112
	v_cvt_pk_bf16_f32 v5, v120, v134
	global_store_dwordx4 v[8:9], v[2:5], off nt
	v_addc_co_u32_e32 v7, vcc, 0, v7, vcc
	s_nop 0
	v_cvt_pk_bf16_f32 v2, v73, v81
	v_cvt_pk_bf16_f32 v3, v89, v97
	v_cvt_pk_bf16_f32 v4, v105, v113
	v_cvt_pk_bf16_f32 v5, v121, v135
	global_store_dwordx4 v[6:7], v[2:5], off nt
	s_branch .LBB0_511

; __device__ __forceinline__ unsigned cvt_pk_bf16(float lo, float hi) { f32x2_t v = {lo, hi}; bf16x2_t b = __builtin_convertvector(v, bf16x2_t); return __builtin_bit_cast(unsigned, b); }
; __device__ __forceinline__ void conv_span128(const float* W, int ldw, int K, bf16* WT, int rowmode, int kb, int n0, int lane) {
;     const int c = lane & 7, nn = lane >> 3;
;     const float* src = W + (size_t)(kb * 64 + 8 * c) * ldw + n0 + 4 * nn;
;     f32x4 v[4][8];
; #pragma unroll
;     for (int h = 0; h < 4; ++h)
; #pragma unroll
;         for (int i = 0; i < 8; ++i) v[h][i] = __builtin_nontemporal_load((const f32x4*)(src + 32 * h + (size_t)i * ldw));
; #pragma unroll
;     for (int h = 0; h < 4; ++h) {
;         const int n = n0 + 32 * h + 4 * nn; int r = n;
;         if (rowmode == 2) r = ((n >> 7) << 8) + (n & 127);
;         else if (rowmode == 3) r = ((n >> 7) << 8) + 128 + (n & 127);
;         bf16* d0 = WT + (size_t)r * K + kb * 64 + 8 * c;
; #pragma unroll
;         for (int j = 0; j < 4; ++j) { u32x4 o; o.x = cvt_pk_bf16(v[h][0][j], v[h][1][j]); o.y = cvt_pk_bf16(v[h][2][j], v[h][3][j]); o.z = cvt_pk_bf16(v[h][4][j], v[h][5][j]); o.w = cvt_pk_bf16(v[h][6][j], v[h][7][j]);
;             *(u32x4*)(d0 + (size_t)j * K) = o; }
;     }
; }
;     ...
;         else { const int e = p / 224, q = p % 224, kb = q >> 1, h = kb / 56;
;             conv_span128(m2 + (size_t)e * FFE * D + (size_t)h * (FFE / 2) * D, 2048, FFE / 2, mdn + (size_t)(e * 2 + h) * D * (FFE / 2), 0, kb - 56 * h, (q & 1) * 1024 + wave * 128, lane); }
.LBB0_996:
	s_or_b64 exec, exec, s[4:5]
	s_and_b32 s6, s18, 0x7fffffff
	s_mov_b64 s[4:5], -1
	s_cmp_lt_i32 s18, 0
	v_lshlrev_b32_e32 v132, 2, v128
	v_lshlrev_b32_e32 v130, 1, v126
	s_cbranch_scc0 .LBB0_998
	s_lshr_b32 s4, s6, 5
	s_mul_hi_u32 s7, s4, 0x24924925
	s_mul_i32 s4, s7, 0xe0
	s_sub_i32 s12, s6, s4
	s_lshr_b32 s13, s12, 1
	s_cmpk_gt_u32 s12, 0x6f
	s_mul_i32 s9, s7, 0x3800000
	v_readlane_b32 s40, v255, 3
	s_cselect_b64 s[4:5], -1, 0
	s_mul_hi_u32 s8, s7, 0x3800000
	v_readlane_b32 s41, v255, 4
	s_add_u32 s14, s40, s9
	s_addc_u32 s15, s41, s8
	s_and_b64 s[8:9], s[4:5], exec
	s_cselect_b32 s8, 0x1c00000, 0
	v_cndmask_b32_e64 v2, 0, 1, s[4:5]
	s_add_u32 s8, s14, s8
	s_addc_u32 s9, s15, 0
	s_lshl_b32 s7, s7, 1
	v_readfirstlane_b32 s14, v2
	s_or_b32 s7, s7, s14
	s_mul_hi_u32 s14, s7, 0xe00000
	s_mul_i32 s7, s7, 0xe00000
	v_readlane_b32 s15, v250, 16
	s_add_u32 s7, s15, s7
	v_readlane_b32 s15, v250, 17
	s_addc_u32 s14, s15, s14
	s_and_b64 s[4:5], s[4:5], exec
	s_cselect_b32 s4, 0xffffffc8, 0
	s_add_i32 s5, s4, s13
	s_lshl_b32 s4, s12, 10
	s_lshl_b32 s12, s5, 6
	v_or_b32_e32 v2, s12, v126
	s_and_b32 s4, s4, 0x400
	v_ashrrev_i32_e32 v3, 31, v2
	s_add_i32 s4, s4, s16
	v_lshlrev_b64 v[2:3], 13, v[2:3]
	v_lshl_add_u64 v[2:3], s[8:9], 0, v[2:3]
	s_ashr_i32 s5, s4, 31
	v_lshl_add_u64 v[2:3], s[4:5], 2, v[2:3]
	v_mov_b32_e32 v133, v187
	v_lshl_add_u64 v[2:3], v[2:3], 0, v[132:133]
	s_movk_i32 s5, 0x2000
	v_add_co_u32_e32 v6, vcc, s5, v2
	s_movk_i32 s5, 0x4000
	s_nop 0
	v_addc_co_u32_e32 v7, vcc, 0, v3, vcc
	v_add_co_u32_e32 v10, vcc, s5, v2
	s_movk_i32 s5, 0x6000
	s_nop 0
	v_addc_co_u32_e32 v11, vcc, 0, v3, vcc
	v_add_co_u32_e32 v14, vcc, s5, v2
	s_mov_b32 s5, 0x8000
	s_nop 0
	v_addc_co_u32_e32 v15, vcc, 0, v3, vcc
	v_add_co_u32_e32 v18, vcc, s5, v2
	s_mov_b32 s5, 0xa000
	s_nop 0
	v_addc_co_u32_e32 v19, vcc, 0, v3, vcc
	v_add_co_u32_e32 v22, vcc, s5, v2
	s_mov_b32 s5, 0xc000
	s_nop 0
	v_addc_co_u32_e32 v23, vcc, 0, v3, vcc
	v_add_co_u32_e32 v26, vcc, s5, v2
	global_load_dwordx4 v[98:101], v[2:3], off nt
	global_load_dwordx4 v[102:105], v[6:7], off nt
	v_addc_co_u32_e32 v27, vcc, 0, v3, vcc
	global_load_dwordx4 v[106:109], v[10:11], off nt
	global_load_dwordx4 v[110:113], v[14:15], off nt
	global_load_dwordx4 v[114:117], v[18:19], off nt
	global_load_dwordx4 v[118:121], v[22:23], off nt
	global_load_dwordx4 v[122:125], v[26:27], off nt
	s_mov_b32 s5, 0xe000
	v_add_co_u32_e32 v30, vcc, s5, v2
	s_ashr_i32 s13, s12, 31
	s_nop 0
	v_addc_co_u32_e32 v31, vcc, 0, v3, vcc
	global_load_dwordx4 v[134:137], v[30:31], off nt
	global_load_dwordx4 v[66:69], v[2:3], off offset:128 nt
	global_load_dwordx4 v[70:73], v[6:7], off offset:128 nt
	global_load_dwordx4 v[74:77], v[10:11], off offset:128 nt
	global_load_dwordx4 v[78:81], v[14:15], off offset:128 nt
	global_load_dwordx4 v[82:85], v[18:19], off offset:128 nt
	global_load_dwordx4 v[86:89], v[22:23], off offset:128 nt
	global_load_dwordx4 v[90:93], v[26:27], off offset:128 nt
	global_load_dwordx4 v[94:97], v[30:31], off offset:128 nt
	global_load_dwordx4 v[34:37], v[2:3], off offset:256 nt
	global_load_dwordx4 v[38:41], v[6:7], off offset:256 nt
	global_load_dwordx4 v[42:45], v[10:11], off offset:256 nt
	global_load_dwordx4 v[46:49], v[14:15], off offset:256 nt
	global_load_dwordx4 v[50:53], v[18:19], off offset:256 nt
	global_load_dwordx4 v[54:57], v[22:23], off offset:256 nt
	global_load_dwordx4 v[58:61], v[26:27], off offset:256 nt
	global_load_dwordx4 v[62:65], v[30:31], off offset:256 nt
	s_nop 0
	global_load_dwordx4 v[2:5], v[2:3], off offset:384 nt
	s_nop 0
	global_load_dwordx4 v[6:9], v[6:7], off offset:384 nt
	s_nop 0
	global_load_dwordx4 v[10:13], v[10:11], off offset:384 nt
	s_nop 0
	global_load_dwordx4 v[14:17], v[14:15], off offset:384 nt
	s_nop 0
	global_load_dwordx4 v[18:21], v[18:19], off offset:384 nt
	s_nop 0
	global_load_dwordx4 v[22:25], v[22:23], off offset:384 nt
	s_nop 0
	global_load_dwordx4 v[26:29], v[26:27], off offset:384 nt
	s_nop 0
	global_load_dwordx4 v[30:33], v[30:31], off offset:384 nt
	v_or_b32_e32 v129, s4, v128
	s_lshl_b64 s[4:5], s[12:13], 1
	s_add_u32 s4, s7, s4
	s_addc_u32 s5, s14, s5
	v_mov_b32_e32 v131, v187
	v_lshl_add_u64 v[142:143], s[4:5], 0, v[130:131]
	s_movk_i32 s8, 0x1c00
	v_mad_i64_i32 v[144:145], s[4:5], v129, s8, v[142:143]
	s_movk_i32 s7, 0x1000
	s_movk_i32 s9, 0x3000
	s_movk_i32 s12, 0x5000
	v_readlane_b32 s42, v255, 5
	v_readlane_b32 s43, v255, 6
	s_movk_i32 s97, 0x1000
	s_waitcnt vmcnt(30)
	v_cvt_pk_bf16_f32 v138, v98, v102
	v_add_co_u32_e32 v98, vcc, s7, v144
	s_waitcnt vmcnt(28)
	v_cvt_pk_bf16_f32 v139, v106, v110
	s_waitcnt vmcnt(26)
	v_cvt_pk_bf16_f32 v140, v114, v118
	s_waitcnt vmcnt(24)
	v_cvt_pk_bf16_f32 v141, v122, v134
	global_store_dwordx4 v[144:145], v[138:141], off nt
	s_nop 1
	v_cvt_pk_bf16_f32 v138, v99, v103
	v_cvt_pk_bf16_f32 v139, v107, v111
	v_cvt_pk_bf16_f32 v140, v115, v119
	v_cvt_pk_bf16_f32 v141, v123, v135
	v_addc_co_u32_e32 v99, vcc, 0, v145, vcc
	global_store_dwordx4 v[98:99], v[138:141], off offset:3072 nt
	v_add_co_u32_e32 v98, vcc, s9, v144
	s_nop 0
	v_cvt_pk_bf16_f32 v138, v100, v104
	v_addc_co_u32_e32 v99, vcc, 0, v145, vcc
	v_cvt_pk_bf16_f32 v139, v108, v112
	v_cvt_pk_bf16_f32 v140, v116, v120
	v_cvt_pk_bf16_f32 v141, v124, v136
	v_add_co_u32_e32 v102, vcc, s12, v144
	global_store_dwordx4 v[98:99], v[138:141], off offset:2048 nt
	v_cvt_pk_bf16_f32 v98, v101, v105
	v_cvt_pk_bf16_f32 v99, v109, v113
	v_cvt_pk_bf16_f32 v100, v117, v121
	v_cvt_pk_bf16_f32 v101, v125, v137
	v_addc_co_u32_e32 v103, vcc, 0, v145, vcc
	global_store_dwordx4 v[102:103], v[98:101], off offset:1024 nt
	s_nop 1
	v_or_b32_e32 v98, 32, v129
	v_mad_i64_i32 v[102:103], s[4:5], v98, s8, v[142:143]
	s_waitcnt vmcnt(26)
; __device__ __forceinline__ unsigned cvt_pk_bf16(float lo, float hi) { f32x2_t v = {lo, hi}; bf16x2_t b = __builtin_convertvector(v, bf16x2_t); return __builtin_bit_cast(unsigned, b); }
; __device__ __forceinline__ void conv_span128(const float* W, int ldw, int K, bf16* WT, int rowmode, int kb, int n0, int lane) {
;     const int c = lane & 7, nn = lane >> 3;
;     const float* src = W + (size_t)(kb * 64 + 8 * c) * ldw + n0 + 4 * nn;
;     f32x4 v[4][8];
; #pragma unroll
;     for (int h = 0; h < 4; ++h)
; #pragma unroll
;         for (int i = 0; i < 8; ++i) v[h][i] = __builtin_nontemporal_load((const f32x4*)(src + 32 * h + (size_t)i * ldw));
; #pragma unroll
;     for (int h = 0; h < 4; ++h) {
;         const int n = n0 + 32 * h + 4 * nn; int r = n;
;         if (rowmode == 2) r = ((n >> 7) << 8) + (n & 127);
;         else if (rowmode == 3) r = ((n >> 7) << 8) + 128 + (n & 127);
;         bf16* d0 = WT + (size_t)r * K + kb * 64 + 8 * c;
; #pragma unroll
;         for (int j = 0; j < 4; ++j) { u32x4 o; o.x = cvt_pk_bf16(v[h][0][j], v[h][1][j]); o.y = cvt_pk_bf16(v[h][2][j], v[h][3][j]); o.z = cvt_pk_bf16(v[h][4][j], v[h][5][j]); o.w = cvt_pk_bf16(v[h][6][j], v[h][7][j]);
;             *(u32x4*)(d0 + (size_t)j * K) = o; }
;     }
; }
;     ...
;         if ((cur >> 31) == 0u) { const int e = p / 448, w3 = (p / 224) & 1, q = p % 224;
;             conv_span128((w3 ? m3 : m1) + (size_t)e * D * FFE, FFE, D, mup + (size_t)e * 2 * FFE * D, 2 + w3, q / 7, (q % 7) * 1024 + wave * 128, lane); }
	v_cvt_pk_bf16_f32 v98, v66, v70
	s_waitcnt vmcnt(24)
	v_cvt_pk_bf16_f32 v99, v74, v78
	s_waitcnt vmcnt(22)
	v_cvt_pk_bf16_f32 v100, v82, v86
	s_waitcnt vmcnt(20)
	v_cvt_pk_bf16_f32 v101, v90, v94
	v_add_co_u32_e32 v66, vcc, s7, v102
	global_store_dwordx4 v[102:103], v[98:101], off nt
	s_nop 1
	v_cvt_pk_bf16_f32 v98, v67, v71
	v_cvt_pk_bf16_f32 v99, v75, v79
	v_cvt_pk_bf16_f32 v100, v83, v87
	v_cvt_pk_bf16_f32 v101, v91, v95
	v_addc_co_u32_e32 v67, vcc, 0, v103, vcc
	global_store_dwordx4 v[66:67], v[98:101], off offset:3072 nt
	v_add_co_u32_e32 v66, vcc, s9, v102
	s_nop 0
	v_cvt_pk_bf16_f32 v98, v68, v72
	v_addc_co_u32_e32 v67, vcc, 0, v103, vcc
	v_cvt_pk_bf16_f32 v99, v76, v80
	v_cvt_pk_bf16_f32 v100, v84, v88
	v_cvt_pk_bf16_f32 v101, v92, v96
	v_add_co_u32_e32 v70, vcc, s12, v102
	global_store_dwordx4 v[66:67], v[98:101], off offset:2048 nt
	v_cvt_pk_bf16_f32 v66, v69, v73
	v_cvt_pk_bf16_f32 v67, v77, v81
	v_cvt_pk_bf16_f32 v68, v85, v89
	v_cvt_pk_bf16_f32 v69, v93, v97
	v_addc_co_u32_e32 v71, vcc, 0, v103, vcc
	global_store_dwordx4 v[70:71], v[66:69], off offset:1024 nt
	s_nop 1
	v_or_b32_e32 v66, 64, v129
	v_mad_i64_i32 v[70:71], s[4:5], v66, s8, v[142:143]
	s_waitcnt vmcnt(22)
	v_cvt_pk_bf16_f32 v66, v34, v38
	s_waitcnt vmcnt(20)
	v_cvt_pk_bf16_f32 v67, v42, v46
	s_waitcnt vmcnt(18)
	v_cvt_pk_bf16_f32 v68, v50, v54
	s_waitcnt vmcnt(16)
	v_cvt_pk_bf16_f32 v69, v58, v62
	v_add_co_u32_e32 v34, vcc, s7, v70
	global_store_dwordx4 v[70:71], v[66:69], off nt
	s_nop 1
	v_cvt_pk_bf16_f32 v66, v35, v39
	v_cvt_pk_bf16_f32 v67, v43, v47
	v_cvt_pk_bf16_f32 v68, v51, v55
	v_cvt_pk_bf16_f32 v69, v59, v63
	v_addc_co_u32_e32 v35, vcc, 0, v71, vcc
	global_store_dwordx4 v[34:35], v[66:69], off offset:3072 nt
	v_add_co_u32_e32 v34, vcc, s9, v70
	s_nop 0
	v_cvt_pk_bf16_f32 v66, v36, v40
	v_addc_co_u32_e32 v35, vcc, 0, v71, vcc
	v_cvt_pk_bf16_f32 v67, v44, v48
	v_cvt_pk_bf16_f32 v68, v52, v56
	v_cvt_pk_bf16_f32 v69, v60, v64
	v_add_co_u32_e32 v38, vcc, s12, v70
	global_store_dwordx4 v[34:35], v[66:69], off offset:2048 nt
	v_cvt_pk_bf16_f32 v34, v37, v41
	v_cvt_pk_bf16_f32 v35, v45, v49
	v_cvt_pk_bf16_f32 v36, v53, v57
	v_cvt_pk_bf16_f32 v37, v61, v65
	v_addc_co_u32_e32 v39, vcc, 0, v71, vcc
	global_store_dwordx4 v[38:39], v[34:37], off offset:1024 nt
	s_nop 1
	v_or_b32_e32 v34, 0x60, v129
	v_mad_i64_i32 v[38:39], s[4:5], v34, s8, v[142:143]
	s_waitcnt vmcnt(18)
	v_cvt_pk_bf16_f32 v34, v2, v6
	s_waitcnt vmcnt(16)
	v_cvt_pk_bf16_f32 v35, v10, v14
	s_waitcnt vmcnt(14)
	v_cvt_pk_bf16_f32 v36, v18, v22
	s_waitcnt vmcnt(12)
	v_cvt_pk_bf16_f32 v37, v26, v30
	v_add_co_u32_e32 v2, vcc, s7, v38
	global_store_dwordx4 v[38:39], v[34:37], off nt
	s_mov_b64 s[4:5], 0
	s_nop 0
	v_cvt_pk_bf16_f32 v34, v3, v7
	v_cvt_pk_bf16_f32 v35, v11, v15
	v_cvt_pk_bf16_f32 v36, v19, v23
	v_cvt_pk_bf16_f32 v37, v27, v31
	v_addc_co_u32_e32 v3, vcc, 0, v39, vcc
	global_store_dwordx4 v[2:3], v[34:37], off offset:3072 nt
	v_add_co_u32_e32 v2, vcc, s9, v38
	s_nop 0
	v_cvt_pk_bf16_f32 v34, v4, v8
	v_addc_co_u32_e32 v3, vcc, 0, v39, vcc
	v_cvt_pk_bf16_f32 v35, v12, v16
	v_cvt_pk_bf16_f32 v36, v20, v24
	v_cvt_pk_bf16_f32 v37, v28, v32
	v_add_co_u32_e32 v6, vcc, 0x5000, v38
	global_store_dwordx4 v[2:3], v[34:37], off offset:2048 nt
	v_cvt_pk_bf16_f32 v2, v5, v9
	v_cvt_pk_bf16_f32 v3, v13, v17
	v_cvt_pk_bf16_f32 v4, v21, v25
	v_cvt_pk_bf16_f32 v5, v29, v33
	v_addc_co_u32_e32 v7, vcc, 0, v39, vcc
	global_store_dwordx4 v[6:7], v[2:5], off offset:1024 nt
.LBB0_998:
	s_andn2_b64 vcc, exec, s[4:5]
	s_cbranch_vccnz .LBB0_986
	s_lshr_b32 s5, s18, 5
	s_mul_hi_u32 s5, s5, 0x24924925
	s_and_b32 s12, s5, 1
	s_mul_hi_u32 s5, s6, 0x92492493
	s_lshr_b32 s5, s5, 7
	s_mulk_i32 s5, 0xe0
	s_lshr_b32 s4, s18, 6
	s_sub_i32 s8, s6, s5
	v_readlane_b32 s40, v255, 7
	s_mul_hi_u32 s4, s4, 0x24924925
	s_cmp_eq_u32 s12, 0
	v_readlane_b32 s44, v255, 11
	v_readlane_b32 s46, v255, 13
	v_readlane_b32 s45, v255, 12
	v_readlane_b32 s47, v255, 14
	s_cselect_b32 s6, s44, s46
	s_mul_hi_u32 s9, s4, 0x3800000
	s_mul_i32 s13, s4, 0x3800000
	s_movk_i32 s4, 0x60
	s_cselect_b32 s7, s45, s47
	s_cselect_b32 s14, 32, 0xa0
	s_cselect_b32 s5, 64, 0xc0
	s_cselect_b32 s4, s4, 0xe0
	s_add_u32 s6, s6, s13
	s_addc_u32 s7, s7, s9
	v_readlane_b32 s15, v250, 14
	s_add_u32 s13, s15, s13
	v_readlane_b32 s15, v250, 15
	s_addc_u32 s9, s15, s9
	s_and_b32 s15, s8, 0xff
	s_mul_i32 s15, s15, 37
	s_lshr_b32 s15, s15, 8
	s_sub_i32 s18, s8, s15
	s_bfe_u32 s18, s18, 0x70001
	s_add_i32 s18, s18, s15
	s_bfe_u32 s15, s18, 0x60002
	v_lshl_or_b32 v2, s15, 6, v126
	s_mul_i32 s18, s15, 7
	v_mul_u32_u24_e32 v186, 0x1c00, v2
	v_lshl_add_u64 v[2:3], v[186:187], 2, s[6:7]
	s_sub_i32 s6, s8, s18
	s_and_b32 s6, s6, 0xff
	s_lshl_b32 s6, s6, 10
	s_add_i32 s6, s6, s16
	s_ashr_i32 s7, s6, 31
	v_lshl_add_u64 v[2:3], s[6:7], 2, v[2:3]
	v_mov_b32_e32 v133, v187
	v_lshl_add_u64 v[70:71], v[2:3], 0, v[132:133]
	s_movk_i32 s7, 0x7000
	v_add_co_u32_e32 v78, vcc, s7, v70
	s_mov_b32 s7, 0xe000
	s_nop 0
	v_addc_co_u32_e32 v79, vcc, 0, v71, vcc
	v_add_co_u32_e32 v86, vcc, s7, v70
	s_mov_b32 s7, 0x15000
	s_nop 0
	v_addc_co_u32_e32 v87, vcc, 0, v71, vcc
	v_add_co_u32_e32 v94, vcc, s7, v70
	s_mov_b32 s7, 0x1c000
	s_nop 0
	v_addc_co_u32_e32 v95, vcc, 0, v71, vcc
	v_add_co_u32_e32 v102, vcc, s7, v70
	s_mov_b32 s7, 0x23000
	s_nop 0
	v_addc_co_u32_e32 v103, vcc, 0, v71, vcc
	v_add_co_u32_e32 v110, vcc, s7, v70
	s_mov_b32 s7, 0x2a000
	s_nop 0
	v_addc_co_u32_e32 v111, vcc, 0, v71, vcc
	v_add_co_u32_e32 v118, vcc, s7, v70
	global_load_dwordx4 v[2:5], v[70:71], off nt
	global_load_dwordx4 v[6:9], v[78:79], off nt
	v_addc_co_u32_e32 v119, vcc, 0, v71, vcc
	global_load_dwordx4 v[10:13], v[86:87], off nt
; __device__ __forceinline__ unsigned cvt_pk_bf16(float lo, float hi) { f32x2_t v = {lo, hi}; bf16x2_t b = __builtin_convertvector(v, bf16x2_t); return __builtin_bit_cast(unsigned, b); }
; __device__ __forceinline__ void conv_span128(const float* W, int ldw, int K, bf16* WT, int rowmode, int kb, int n0, int lane) {
;     const int c = lane & 7, nn = lane >> 3;
;     const float* src = W + (size_t)(kb * 64 + 8 * c) * ldw + n0 + 4 * nn;
;     f32x4 v[4][8];
; #pragma unroll
;     for (int h = 0; h < 4; ++h)
; #pragma unroll
;         for (int i = 0; i < 8; ++i) v[h][i] = __builtin_nontemporal_load((const f32x4*)(src + 32 * h + (size_t)i * ldw));
; #pragma unroll
;     for (int h = 0; h < 4; ++h) {
;         const int n = n0 + 32 * h + 4 * nn; int r = n;
;         if (rowmode == 2) r = ((n >> 7) << 8) + (n & 127);
;         else if (rowmode == 3) r = ((n >> 7) << 8) + 128 + (n & 127);
;         bf16* d0 = WT + (size_t)r * K + kb * 64 + 8 * c;
; #pragma unroll
;         for (int j = 0; j < 4; ++j) { u32x4 o; o.x = cvt_pk_bf16(v[h][0][j], v[h][1][j]); o.y = cvt_pk_bf16(v[h][2][j], v[h][3][j]); o.z = cvt_pk_bf16(v[h][4][j], v[h][5][j]); o.w = cvt_pk_bf16(v[h][6][j], v[h][7][j]);
;             *(u32x4*)(d0 + (size_t)j * K) = o; }
;     }
; }
	global_load_dwordx4 v[14:17], v[94:95], off nt
	global_load_dwordx4 v[18:21], v[102:103], off nt
	global_load_dwordx4 v[22:25], v[110:111], off nt
	global_load_dwordx4 v[26:29], v[118:119], off nt
	s_mov_b32 s7, 0x31000
	v_add_co_u32_e32 v132, vcc, s7, v70
	s_lshl_b32 s7, s15, 7
	s_nop 0
	v_addc_co_u32_e32 v133, vcc, 0, v71, vcc
	global_load_dwordx4 v[30:33], v[132:133], off nt
	global_load_dwordx4 v[34:37], v[70:71], off offset:128 nt
	global_load_dwordx4 v[38:41], v[78:79], off offset:128 nt
	global_load_dwordx4 v[42:45], v[86:87], off offset:128 nt
	global_load_dwordx4 v[46:49], v[94:95], off offset:128 nt
	global_load_dwordx4 v[50:53], v[102:103], off offset:128 nt
	global_load_dwordx4 v[54:57], v[110:111], off offset:128 nt
	global_load_dwordx4 v[58:61], v[118:119], off offset:128 nt
	global_load_dwordx4 v[62:65], v[132:133], off offset:128 nt
	global_load_dwordx4 v[66:69], v[70:71], off offset:256 nt
	s_nop 0
	global_load_dwordx4 v[70:73], v[70:71], off offset:384 nt
	s_nop 0
	global_load_dwordx4 v[74:77], v[78:79], off offset:256 nt
	s_nop 0
	global_load_dwordx4 v[78:81], v[78:79], off offset:384 nt
	s_nop 0
	global_load_dwordx4 v[82:85], v[86:87], off offset:256 nt
	s_nop 0
	global_load_dwordx4 v[86:89], v[86:87], off offset:384 nt
	s_nop 0
	global_load_dwordx4 v[90:93], v[94:95], off offset:256 nt
	s_nop 0
	global_load_dwordx4 v[94:97], v[94:95], off offset:384 nt
	s_nop 0
	global_load_dwordx4 v[98:101], v[102:103], off offset:256 nt
	s_nop 0
	global_load_dwordx4 v[102:105], v[102:103], off offset:384 nt
	s_nop 0
	global_load_dwordx4 v[106:109], v[110:111], off offset:256 nt
	s_nop 0
	global_load_dwordx4 v[110:113], v[110:111], off offset:384 nt
	s_nop 0
	global_load_dwordx4 v[114:117], v[118:119], off offset:256 nt
	s_nop 0
	global_load_dwordx4 v[118:121], v[118:119], off offset:384 nt
	s_nop 0
	global_load_dwordx4 v[122:125], v[132:133], off offset:256 nt
	s_nop 0
	global_load_dwordx4 v[132:135], v[132:133], off offset:384 nt
	s_add_u32 s8, s13, s7
	s_addc_u32 s9, s9, 0
	s_lshl_b32 s6, s6, 1
	v_lshl_or_b32 v129, s12, 7, v128
	v_or_b32_e32 v136, s6, v129
	v_mov_b32_e32 v131, v187
	v_ashrrev_i32_e32 v137, 31, v136
	v_lshl_add_u64 v[130:131], s[8:9], 0, v[130:131]
	v_lshlrev_b64 v[136:137], 12, v[136:137]
	v_lshl_add_u64 v[140:141], v[130:131], 0, v[136:137]
	s_movk_i32 s7, 0x2000
	s_movk_i32 s8, 0x3000
	v_readlane_b32 s41, v255, 8
	v_readlane_b32 s42, v255, 9
	v_readlane_b32 s43, v255, 10
	s_waitcnt vmcnt(30)
	v_cvt_pk_bf16_f32 v136, v2, v6
	v_add_co_u32_e32 v2, vcc, s7, v140
	s_waitcnt vmcnt(28)
	v_cvt_pk_bf16_f32 v137, v10, v14
	s_waitcnt vmcnt(26)
	v_cvt_pk_bf16_f32 v138, v18, v22
	s_waitcnt vmcnt(24)
	v_cvt_pk_bf16_f32 v139, v26, v30
	global_store_dwordx4 v[140:141], v[136:139], off nt
	s_nop 1
	v_cvt_pk_bf16_f32 v136, v3, v7
	v_cvt_pk_bf16_f32 v137, v11, v15
	v_cvt_pk_bf16_f32 v138, v19, v23
	v_cvt_pk_bf16_f32 v139, v27, v31
	v_addc_co_u32_e32 v3, vcc, 0, v141, vcc
	global_store_dwordx4 v[2:3], v[136:139], off offset:-4096 nt
	v_add_co_u32_e32 v6, vcc, s8, v140
	s_nop 0
	v_cvt_pk_bf16_f32 v136, v4, v8
	v_cvt_pk_bf16_f32 v137, v12, v16
	v_cvt_pk_bf16_f32 v138, v20, v24
	v_cvt_pk_bf16_f32 v139, v28, v32
	global_store_dwordx4 v[2:3], v[136:139], off nt
	v_cvt_pk_bf16_f32 v2, v5, v9
	v_cvt_pk_bf16_f32 v3, v13, v17
	v_cvt_pk_bf16_f32 v4, v21, v25
	v_cvt_pk_bf16_f32 v5, v29, v33
	v_addc_co_u32_e32 v7, vcc, 0, v141, vcc
	global_store_dwordx4 v[6:7], v[2:5], off nt
	s_nop 1
	v_or_b32_e32 v2, s14, v128
	v_or_b32_e32 v2, s6, v2
	v_ashrrev_i32_e32 v3, 31, v2
	v_lshlrev_b64 v[2:3], 12, v[2:3]
	v_lshl_add_u64 v[6:7], v[130:131], 0, v[2:3]
	s_waitcnt vmcnt(26)
	v_cvt_pk_bf16_f32 v2, v34, v38
	s_waitcnt vmcnt(24)
	v_cvt_pk_bf16_f32 v3, v42, v46
	s_waitcnt vmcnt(22)
	v_cvt_pk_bf16_f32 v4, v50, v54
	s_waitcnt vmcnt(20)
	v_cvt_pk_bf16_f32 v5, v58, v62
	v_add_co_u32_e32 v8, vcc, s7, v6
	global_store_dwordx4 v[6:7], v[2:5], off nt
	s_nop 0
	v_addc_co_u32_e32 v9, vcc, 0, v7, vcc
	v_cvt_pk_bf16_f32 v2, v35, v39
	v_cvt_pk_bf16_f32 v3, v43, v47
	v_cvt_pk_bf16_f32 v4, v51, v55
	v_cvt_pk_bf16_f32 v5, v59, v63
	global_store_dwordx4 v[8:9], v[2:5], off offset:-4096 nt
	v_add_co_u32_e32 v6, vcc, s8, v6
	s_nop 0
	v_cvt_pk_bf16_f32 v2, v36, v40
	v_cvt_pk_bf16_f32 v3, v44, v48
	v_cvt_pk_bf16_f32 v4, v52, v56
	v_cvt_pk_bf16_f32 v5, v60, v64
	global_store_dwordx4 v[8:9], v[2:5], off nt
	v_addc_co_u32_e32 v7, vcc, 0, v7, vcc
	s_nop 0
	v_cvt_pk_bf16_f32 v2, v37, v41
	v_cvt_pk_bf16_f32 v3, v45, v49
	v_cvt_pk_bf16_f32 v4, v53, v57
	v_cvt_pk_bf16_f32 v5, v61, v65
	global_store_dwordx4 v[6:7], v[2:5], off nt
	s_nop 1
	v_or_b32_e32 v2, s5, v128
	v_or_b32_e32 v2, s6, v2
	v_ashrrev_i32_e32 v3, 31, v2
	v_lshlrev_b64 v[2:3], 12, v[2:3]
	v_lshl_add_u64 v[6:7], v[130:131], 0, v[2:3]
	s_waitcnt vmcnt(21)
	v_cvt_pk_bf16_f32 v2, v66, v74
	s_waitcnt vmcnt(17)
	v_cvt_pk_bf16_f32 v3, v82, v90
	s_waitcnt vmcnt(13)
	v_cvt_pk_bf16_f32 v4, v98, v106
	s_waitcnt vmcnt(9)
	v_cvt_pk_bf16_f32 v5, v114, v122
	v_add_co_u32_e32 v8, vcc, s7, v6
	global_store_dwordx4 v[6:7], v[2:5], off nt
	s_nop 0
	v_addc_co_u32_e32 v9, vcc, 0, v7, vcc
	v_cvt_pk_bf16_f32 v2, v67, v75
	v_cvt_pk_bf16_f32 v3, v83, v91
	v_cvt_pk_bf16_f32 v4, v99, v107
	v_cvt_pk_bf16_f32 v5, v115, v123
	global_store_dwordx4 v[8:9], v[2:5], off offset:-4096 nt
	v_add_co_u32_e32 v6, vcc, s8, v6
	s_nop 0
	v_cvt_pk_bf16_f32 v2, v68, v76
	v_cvt_pk_bf16_f32 v3, v84, v92
	v_cvt_pk_bf16_f32 v4, v100, v108
	v_cvt_pk_bf16_f32 v5, v116, v124
	global_store_dwordx4 v[8:9], v[2:5], off nt
	v_addc_co_u32_e32 v7, vcc, 0, v7, vcc
	s_nop 0
	v_cvt_pk_bf16_f32 v2, v69, v77
	v_cvt_pk_bf16_f32 v3, v85, v93
	v_cvt_pk_bf16_f32 v4, v101, v109
	v_cvt_pk_bf16_f32 v5, v117, v125
	global_store_dwordx4 v[6:7], v[2:5], off nt
	s_nop 1
	v_or_b32_e32 v2, s4, v128
	v_or_b32_e32 v2, s6, v2
	v_ashrrev_i32_e32 v3, 31, v2
	v_lshlrev_b64 v[2:3], 12, v[2:3]
	v_lshl_add_u64 v[6:7], v[130:131], 0, v[2:3]
	v_cvt_pk_bf16_f32 v2, v70, v78
	v_cvt_pk_bf16_f32 v3, v86, v94
	v_cvt_pk_bf16_f32 v4, v102, v110
	s_waitcnt vmcnt(12)
	v_cvt_pk_bf16_f32 v5, v118, v132
	v_add_co_u32_e32 v8, vcc, s7, v6
	global_store_dwordx4 v[6:7], v[2:5], off nt
	s_nop 0
	v_addc_co_u32_e32 v9, vcc, 0, v7, vcc
	v_cvt_pk_bf16_f32 v2, v71, v79
	v_cvt_pk_bf16_f32 v3, v87, v95
	v_cvt_pk_bf16_f32 v4, v103, v111
	v_cvt_pk_bf16_f32 v5, v119, v133
	global_store_dwordx4 v[8:9], v[2:5], off offset:-4096 nt
	v_add_co_u32_e32 v6, vcc, 0x3000, v6
	s_nop 0
	v_cvt_pk_bf16_f32 v2, v72, v80
	v_cvt_pk_bf16_f32 v3, v88, v96
	v_cvt_pk_bf16_f32 v4, v104, v112
	v_cvt_pk_bf16_f32 v5, v120, v134
	global_store_dwordx4 v[8:9], v[2:5], off nt
	v_addc_co_u32_e32 v7, vcc, 0, v7, vcc
	s_nop 0
	v_cvt_pk_bf16_f32 v2, v73, v81
	v_cvt_pk_bf16_f32 v3, v89, v97
	v_cvt_pk_bf16_f32 v4, v105, v113
	v_cvt_pk_bf16_f32 v5, v121, v135
	global_store_dwordx4 v[6:7], v[2:5], off nt
	s_branch .LBB0_986

; __device__ __forceinline__ unsigned cvt_pk_bf16(float lo, float hi) { f32x2_t v = {lo, hi}; bf16x2_t b = __builtin_convertvector(v, bf16x2_t); return __builtin_bit_cast(unsigned, b); }
; __device__ __forceinline__ void conv_span128(const float* W, int ldw, int K, bf16* WT, int rowmode, int kb, int n0, int lane) {
;     const int c = lane & 7, nn = lane >> 3;
;     const float* src = W + (size_t)(kb * 64 + 8 * c) * ldw + n0 + 4 * nn;
;     f32x4 v[4][8];
; #pragma unroll
;     for (int h = 0; h < 4; ++h)
; #pragma unroll
;         for (int i = 0; i < 8; ++i) v[h][i] = __builtin_nontemporal_load((const f32x4*)(src + 32 * h + (size_t)i * ldw));
; #pragma unroll
;     for (int h = 0; h < 4; ++h) {
;         const int n = n0 + 32 * h + 4 * nn; int r = n;
;         if (rowmode == 2) r = ((n >> 7) << 8) + (n & 127);
;         else if (rowmode == 3) r = ((n >> 7) << 8) + 128 + (n & 127);
;         bf16* d0 = WT + (size_t)r * K + kb * 64 + 8 * c;
; #pragma unroll
;         for (int j = 0; j < 4; ++j) { u32x4 o; o.x = cvt_pk_bf16(v[h][0][j], v[h][1][j]); o.y = cvt_pk_bf16(v[h][2][j], v[h][3][j]); o.z = cvt_pk_bf16(v[h][4][j], v[h][5][j]); o.w = cvt_pk_bf16(v[h][6][j], v[h][7][j]);
;             *(u32x4*)(d0 + (size_t)j * K) = o; }
;     }
; }
;     ...
;         else { const int e = p / 224, q = p % 224, kb = q >> 1, h = kb / 56;
;             conv_span128(m2 + (size_t)e * FFE * D + (size_t)h * (FFE / 2) * D, 2048, FFE / 2, mdn + (size_t)(e * 2 + h) * D * (FFE / 2), 0, kb - 56 * h, (q & 1) * 1024 + wave * 128, lane); }
.LBB0_1081:
	s_or_b64 exec, exec, s[4:5]
	s_and_b32 s6, s18, 0x7fffffff
	s_mov_b64 s[4:5], -1
	s_cmp_lt_i32 s18, 0
	v_lshlrev_b32_e32 v132, 2, v128
	v_lshlrev_b32_e32 v130, 1, v126
	s_cbranch_scc0 .LBB0_1083
	s_lshr_b32 s4, s6, 5
	s_mul_hi_u32 s7, s4, 0x24924925
	s_mul_i32 s4, s7, 0xe0
	s_sub_i32 s10, s6, s4
	s_lshr_b32 s11, s10, 1
	s_cmpk_gt_u32 s10, 0x6f
	s_mul_i32 s9, s7, 0x3800000
	v_readlane_b32 s12, v255, 3
	s_cselect_b64 s[4:5], -1, 0
	s_mul_hi_u32 s8, s7, 0x3800000
	v_readlane_b32 s13, v255, 4
	s_add_u32 s12, s12, s9
	s_addc_u32 s13, s13, s8
	s_and_b64 s[8:9], s[4:5], exec
	s_cselect_b32 s8, 0x1c00000, 0
	v_cndmask_b32_e64 v2, 0, 1, s[4:5]
	s_add_u32 s8, s12, s8
	s_addc_u32 s9, s13, 0
	s_lshl_b32 s7, s7, 1
	v_readfirstlane_b32 s12, v2
	s_or_b32 s7, s7, s12
	s_mul_hi_u32 s12, s7, 0xe00000
	s_mul_i32 s7, s7, 0xe00000
	v_readlane_b32 s13, v250, 16
	s_add_u32 s7, s13, s7
	v_readlane_b32 s13, v250, 17
	s_addc_u32 s12, s13, s12
	s_and_b64 s[4:5], s[4:5], exec
	s_cselect_b32 s4, 0xffffffc8, 0
	s_add_i32 s5, s4, s11
	s_lshl_b32 s4, s10, 10
	s_lshl_b32 s10, s5, 6
	v_or_b32_e32 v2, s10, v126
	s_and_b32 s4, s4, 0x400
	v_ashrrev_i32_e32 v3, 31, v2
	s_add_i32 s4, s4, s16
	v_lshlrev_b64 v[2:3], 13, v[2:3]
	v_lshl_add_u64 v[2:3], s[8:9], 0, v[2:3]
	s_ashr_i32 s5, s4, 31
	v_lshl_add_u64 v[2:3], s[4:5], 2, v[2:3]
	v_mov_b32_e32 v133, v187
	v_lshl_add_u64 v[2:3], v[2:3], 0, v[132:133]
	s_movk_i32 s5, 0x2000
	v_add_co_u32_e32 v6, vcc, s5, v2
	s_movk_i32 s5, 0x4000
	s_nop 0
	v_addc_co_u32_e32 v7, vcc, 0, v3, vcc
	v_add_co_u32_e32 v10, vcc, s5, v2
	s_movk_i32 s5, 0x6000
	s_nop 0
	v_addc_co_u32_e32 v11, vcc, 0, v3, vcc
	v_add_co_u32_e32 v14, vcc, s5, v2
	s_mov_b32 s5, 0x8000
	s_nop 0
	v_addc_co_u32_e32 v15, vcc, 0, v3, vcc
	v_add_co_u32_e32 v18, vcc, s5, v2
	s_mov_b32 s5, 0xa000
	s_nop 0
	v_addc_co_u32_e32 v19, vcc, 0, v3, vcc
	v_add_co_u32_e32 v22, vcc, s5, v2
	s_mov_b32 s5, 0xc000
	s_nop 0
	v_addc_co_u32_e32 v23, vcc, 0, v3, vcc
	v_add_co_u32_e32 v26, vcc, s5, v2
	global_load_dwordx4 v[98:101], v[2:3], off nt
	global_load_dwordx4 v[102:105], v[6:7], off nt
	v_addc_co_u32_e32 v27, vcc, 0, v3, vcc
	global_load_dwordx4 v[106:109], v[10:11], off nt
	global_load_dwordx4 v[110:113], v[14:15], off nt
	global_load_dwordx4 v[114:117], v[18:19], off nt
	global_load_dwordx4 v[118:121], v[22:23], off nt
	global_load_dwordx4 v[122:125], v[26:27], off nt
	s_mov_b32 s5, 0xe000
	v_add_co_u32_e32 v30, vcc, s5, v2
	s_ashr_i32 s11, s10, 31
	s_nop 0
	v_addc_co_u32_e32 v31, vcc, 0, v3, vcc
	global_load_dwordx4 v[134:137], v[30:31], off nt
	global_load_dwordx4 v[66:69], v[2:3], off offset:128 nt
	global_load_dwordx4 v[70:73], v[6:7], off offset:128 nt
	global_load_dwordx4 v[74:77], v[10:11], off offset:128 nt
	global_load_dwordx4 v[78:81], v[14:15], off offset:128 nt
	global_load_dwordx4 v[82:85], v[18:19], off offset:128 nt
	global_load_dwordx4 v[86:89], v[22:23], off offset:128 nt
	global_load_dwordx4 v[90:93], v[26:27], off offset:128 nt
	global_load_dwordx4 v[94:97], v[30:31], off offset:128 nt
	global_load_dwordx4 v[34:37], v[2:3], off offset:256 nt
	global_load_dwordx4 v[38:41], v[6:7], off offset:256 nt
	global_load_dwordx4 v[42:45], v[10:11], off offset:256 nt
	global_load_dwordx4 v[46:49], v[14:15], off offset:256 nt
	global_load_dwordx4 v[50:53], v[18:19], off offset:256 nt
	global_load_dwordx4 v[54:57], v[22:23], off offset:256 nt
	global_load_dwordx4 v[58:61], v[26:27], off offset:256 nt
	global_load_dwordx4 v[62:65], v[30:31], off offset:256 nt
	s_nop 0
	global_load_dwordx4 v[2:5], v[2:3], off offset:384 nt
	s_nop 0
	global_load_dwordx4 v[6:9], v[6:7], off offset:384 nt
	s_nop 0
	global_load_dwordx4 v[10:13], v[10:11], off offset:384 nt
	s_nop 0
	global_load_dwordx4 v[14:17], v[14:15], off offset:384 nt
	s_nop 0
	global_load_dwordx4 v[18:21], v[18:19], off offset:384 nt
	s_nop 0
	global_load_dwordx4 v[22:25], v[22:23], off offset:384 nt
	s_nop 0
	global_load_dwordx4 v[26:29], v[26:27], off offset:384 nt
	s_nop 0
	global_load_dwordx4 v[30:33], v[30:31], off offset:384 nt
	v_or_b32_e32 v133, s4, v128
	s_lshl_b64 s[4:5], s[10:11], 1
	s_add_u32 s4, s7, s4
	s_addc_u32 s5, s12, s5
	v_mov_b32_e32 v131, v187
	v_lshl_add_u64 v[142:143], s[4:5], 0, v[130:131]
	s_movk_i32 s8, 0x1c00
	v_mad_i64_i32 v[144:145], s[4:5], v133, s8, v[142:143]
	s_movk_i32 s7, 0x1000
	s_movk_i32 s9, 0x3000
	s_movk_i32 s10, 0x5000
	v_readlane_b32 s14, v255, 5
	v_readlane_b32 s15, v255, 6
	s_movk_i32 s97, 0x1000
	s_waitcnt vmcnt(30)
	v_cvt_pk_bf16_f32 v138, v98, v102
	v_add_co_u32_e32 v98, vcc, s7, v144
	s_waitcnt vmcnt(28)
	v_cvt_pk_bf16_f32 v139, v106, v110
	s_waitcnt vmcnt(26)
	v_cvt_pk_bf16_f32 v140, v114, v118
	s_waitcnt vmcnt(24)
	v_cvt_pk_bf16_f32 v141, v122, v134
	global_store_dwordx4 v[144:145], v[138:141], off nt
	s_nop 1
	v_cvt_pk_bf16_f32 v138, v99, v103
	v_cvt_pk_bf16_f32 v139, v107, v111
	v_cvt_pk_bf16_f32 v140, v115, v119
	v_cvt_pk_bf16_f32 v141, v123, v135
	v_addc_co_u32_e32 v99, vcc, 0, v145, vcc
	global_store_dwordx4 v[98:99], v[138:141], off offset:3072 nt
	v_add_co_u32_e32 v98, vcc, s9, v144
	s_nop 0
	v_cvt_pk_bf16_f32 v138, v100, v104
	v_addc_co_u32_e32 v99, vcc, 0, v145, vcc
	v_cvt_pk_bf16_f32 v139, v108, v112
	v_cvt_pk_bf16_f32 v140, v116, v120
	v_cvt_pk_bf16_f32 v141, v124, v136
	v_add_co_u32_e32 v102, vcc, s10, v144
	global_store_dwordx4 v[98:99], v[138:141], off offset:2048 nt
	v_cvt_pk_bf16_f32 v98, v101, v105
	v_cvt_pk_bf16_f32 v99, v109, v113
	v_cvt_pk_bf16_f32 v100, v117, v121
	v_cvt_pk_bf16_f32 v101, v125, v137
	v_addc_co_u32_e32 v103, vcc, 0, v145, vcc
	global_store_dwordx4 v[102:103], v[98:101], off offset:1024 nt
	s_nop 1
	v_or_b32_e32 v98, 32, v133
	v_mad_i64_i32 v[102:103], s[4:5], v98, s8, v[142:143]
	s_waitcnt vmcnt(26)
; __device__ __forceinline__ unsigned cvt_pk_bf16(float lo, float hi) { f32x2_t v = {lo, hi}; bf16x2_t b = __builtin_convertvector(v, bf16x2_t); return __builtin_bit_cast(unsigned, b); }
; __device__ __forceinline__ void conv_span128(const float* W, int ldw, int K, bf16* WT, int rowmode, int kb, int n0, int lane) {
;     const int c = lane & 7, nn = lane >> 3;
;     const float* src = W + (size_t)(kb * 64 + 8 * c) * ldw + n0 + 4 * nn;
;     f32x4 v[4][8];
; #pragma unroll
;     for (int h = 0; h < 4; ++h)
; #pragma unroll
;         for (int i = 0; i < 8; ++i) v[h][i] = __builtin_nontemporal_load((const f32x4*)(src + 32 * h + (size_t)i * ldw));
; #pragma unroll
;     for (int h = 0; h < 4; ++h) {
;         const int n = n0 + 32 * h + 4 * nn; int r = n;
;         if (rowmode == 2) r = ((n >> 7) << 8) + (n & 127);
;         else if (rowmode == 3) r = ((n >> 7) << 8) + 128 + (n & 127);
;         bf16* d0 = WT + (size_t)r * K + kb * 64 + 8 * c;
; #pragma unroll
;         for (int j = 0; j < 4; ++j) { u32x4 o; o.x = cvt_pk_bf16(v[h][0][j], v[h][1][j]); o.y = cvt_pk_bf16(v[h][2][j], v[h][3][j]); o.z = cvt_pk_bf16(v[h][4][j], v[h][5][j]); o.w = cvt_pk_bf16(v[h][6][j], v[h][7][j]);
;             *(u32x4*)(d0 + (size_t)j * K) = o; }
;     }
; }
;     ...
;         if ((cur >> 31) == 0u) { const int e = p / 448, w3 = (p / 224) & 1, q = p % 224;
;             conv_span128((w3 ? m3 : m1) + (size_t)e * D * FFE, FFE, D, mup + (size_t)e * 2 * FFE * D, 2 + w3, q / 7, (q % 7) * 1024 + wave * 128, lane); }
	v_cvt_pk_bf16_f32 v98, v66, v70
	s_waitcnt vmcnt(24)
	v_cvt_pk_bf16_f32 v99, v74, v78
	s_waitcnt vmcnt(22)
	v_cvt_pk_bf16_f32 v100, v82, v86
	s_waitcnt vmcnt(20)
	v_cvt_pk_bf16_f32 v101, v90, v94
	v_add_co_u32_e32 v66, vcc, s7, v102
	global_store_dwordx4 v[102:103], v[98:101], off nt
	s_nop 1
	v_cvt_pk_bf16_f32 v98, v67, v71
	v_cvt_pk_bf16_f32 v99, v75, v79
	v_cvt_pk_bf16_f32 v100, v83, v87
	v_cvt_pk_bf16_f32 v101, v91, v95
	v_addc_co_u32_e32 v67, vcc, 0, v103, vcc
	global_store_dwordx4 v[66:67], v[98:101], off offset:3072 nt
	v_add_co_u32_e32 v66, vcc, s9, v102
	s_nop 0
	v_cvt_pk_bf16_f32 v98, v68, v72
	v_addc_co_u32_e32 v67, vcc, 0, v103, vcc
	v_cvt_pk_bf16_f32 v99, v76, v80
	v_cvt_pk_bf16_f32 v100, v84, v88
	v_cvt_pk_bf16_f32 v101, v92, v96
	v_add_co_u32_e32 v70, vcc, s10, v102
	global_store_dwordx4 v[66:67], v[98:101], off offset:2048 nt
	v_cvt_pk_bf16_f32 v66, v69, v73
	v_cvt_pk_bf16_f32 v67, v77, v81
	v_cvt_pk_bf16_f32 v68, v85, v89
	v_cvt_pk_bf16_f32 v69, v93, v97
	v_addc_co_u32_e32 v71, vcc, 0, v103, vcc
	global_store_dwordx4 v[70:71], v[66:69], off offset:1024 nt
	s_nop 1
	v_or_b32_e32 v66, 64, v133
	v_mad_i64_i32 v[70:71], s[4:5], v66, s8, v[142:143]
	s_waitcnt vmcnt(22)
	v_cvt_pk_bf16_f32 v66, v34, v38
	s_waitcnt vmcnt(20)
	v_cvt_pk_bf16_f32 v67, v42, v46
	s_waitcnt vmcnt(18)
	v_cvt_pk_bf16_f32 v68, v50, v54
	s_waitcnt vmcnt(16)
	v_cvt_pk_bf16_f32 v69, v58, v62
	v_add_co_u32_e32 v34, vcc, s7, v70
	global_store_dwordx4 v[70:71], v[66:69], off nt
	s_nop 1
	v_cvt_pk_bf16_f32 v66, v35, v39
	v_cvt_pk_bf16_f32 v67, v43, v47
	v_cvt_pk_bf16_f32 v68, v51, v55
	v_cvt_pk_bf16_f32 v69, v59, v63
	v_addc_co_u32_e32 v35, vcc, 0, v71, vcc
	global_store_dwordx4 v[34:35], v[66:69], off offset:3072 nt
	v_add_co_u32_e32 v34, vcc, s9, v70
	s_nop 0
	v_cvt_pk_bf16_f32 v66, v36, v40
	v_addc_co_u32_e32 v35, vcc, 0, v71, vcc
	v_cvt_pk_bf16_f32 v67, v44, v48
	v_cvt_pk_bf16_f32 v68, v52, v56
	v_cvt_pk_bf16_f32 v69, v60, v64
	v_add_co_u32_e32 v38, vcc, s10, v70
	global_store_dwordx4 v[34:35], v[66:69], off offset:2048 nt
	v_cvt_pk_bf16_f32 v34, v37, v41
	v_cvt_pk_bf16_f32 v35, v45, v49
	v_cvt_pk_bf16_f32 v36, v53, v57
	v_cvt_pk_bf16_f32 v37, v61, v65
	v_addc_co_u32_e32 v39, vcc, 0, v71, vcc
	global_store_dwordx4 v[38:39], v[34:37], off offset:1024 nt
	s_nop 1
	v_or_b32_e32 v34, 0x60, v133
	v_mad_i64_i32 v[38:39], s[4:5], v34, s8, v[142:143]
	s_waitcnt vmcnt(18)
	v_cvt_pk_bf16_f32 v34, v2, v6
	s_waitcnt vmcnt(16)
	v_cvt_pk_bf16_f32 v35, v10, v14
	s_waitcnt vmcnt(14)
	v_cvt_pk_bf16_f32 v36, v18, v22
	s_waitcnt vmcnt(12)
	v_cvt_pk_bf16_f32 v37, v26, v30
	v_add_co_u32_e32 v2, vcc, s7, v38
	global_store_dwordx4 v[38:39], v[34:37], off nt
	s_mov_b64 s[4:5], 0
	s_nop 0
	v_cvt_pk_bf16_f32 v34, v3, v7
	v_cvt_pk_bf16_f32 v35, v11, v15
	v_cvt_pk_bf16_f32 v36, v19, v23
	v_cvt_pk_bf16_f32 v37, v27, v31
	v_addc_co_u32_e32 v3, vcc, 0, v39, vcc
	global_store_dwordx4 v[2:3], v[34:37], off offset:3072 nt
	v_add_co_u32_e32 v2, vcc, s9, v38
	s_nop 0
	v_cvt_pk_bf16_f32 v34, v4, v8
	v_addc_co_u32_e32 v3, vcc, 0, v39, vcc
	v_cvt_pk_bf16_f32 v35, v12, v16
	v_cvt_pk_bf16_f32 v36, v20, v24
	v_cvt_pk_bf16_f32 v37, v28, v32
	v_add_co_u32_e32 v6, vcc, 0x5000, v38
	global_store_dwordx4 v[2:3], v[34:37], off offset:2048 nt
	v_cvt_pk_bf16_f32 v2, v5, v9
	v_cvt_pk_bf16_f32 v3, v13, v17
	v_cvt_pk_bf16_f32 v4, v21, v25
	v_cvt_pk_bf16_f32 v5, v29, v33
	v_addc_co_u32_e32 v7, vcc, 0, v39, vcc
	global_store_dwordx4 v[6:7], v[2:5], off offset:1024 nt
.LBB0_1083:
	s_andn2_b64 vcc, exec, s[4:5]
	s_cbranch_vccnz .LBB0_1065
	s_lshr_b32 s5, s18, 5
	s_mul_hi_u32 s5, s5, 0x24924925
	s_and_b32 s10, s5, 1
	s_mul_hi_u32 s5, s6, 0x92492493
	s_lshr_b32 s5, s5, 7
	s_mulk_i32 s5, 0xe0
	s_lshr_b32 s4, s18, 6
	s_sub_i32 s8, s6, s5
	v_readlane_b32 s40, v255, 7
	s_mul_hi_u32 s4, s4, 0x24924925
	s_cmp_eq_u32 s10, 0
	v_readlane_b32 s44, v255, 11
	v_readlane_b32 s46, v255, 13
	v_readlane_b32 s45, v255, 12
	v_readlane_b32 s47, v255, 14
	s_cselect_b32 s6, s44, s46
	s_mul_hi_u32 s9, s4, 0x3800000
	s_mul_i32 s11, s4, 0x3800000
	s_movk_i32 s4, 0x60
	s_cselect_b32 s7, s45, s47
	s_cselect_b32 s12, 32, 0xa0
	s_cselect_b32 s5, 64, 0xc0
	s_cselect_b32 s4, s4, 0xe0
	s_add_u32 s6, s6, s11
	s_addc_u32 s7, s7, s9
	v_readlane_b32 s13, v250, 14
	s_add_u32 s11, s13, s11
	v_readlane_b32 s13, v250, 15
	s_addc_u32 s9, s13, s9
	s_and_b32 s13, s8, 0xff
	s_mul_i32 s13, s13, 37
	s_lshr_b32 s13, s13, 8
	s_sub_i32 s14, s8, s13
	s_bfe_u32 s14, s14, 0x70001
	s_add_i32 s14, s14, s13
	s_bfe_u32 s13, s14, 0x60002
	v_lshl_or_b32 v2, s13, 6, v126
	s_mul_i32 s14, s13, 7
	v_mul_u32_u24_e32 v186, 0x1c00, v2
	v_lshl_add_u64 v[2:3], v[186:187], 2, s[6:7]
	s_sub_i32 s6, s8, s14
	s_and_b32 s6, s6, 0xff
	s_lshl_b32 s6, s6, 10
	s_add_i32 s6, s6, s16
	s_ashr_i32 s7, s6, 31
	v_lshl_add_u64 v[2:3], s[6:7], 2, v[2:3]
	v_mov_b32_e32 v133, v187
	v_lshl_add_u64 v[70:71], v[2:3], 0, v[132:133]
	s_movk_i32 s7, 0x7000
	v_add_co_u32_e32 v78, vcc, s7, v70
	s_mov_b32 s7, 0xe000
	s_nop 0
	v_addc_co_u32_e32 v79, vcc, 0, v71, vcc
	v_add_co_u32_e32 v86, vcc, s7, v70
	s_mov_b32 s7, 0x15000
	s_nop 0
	v_addc_co_u32_e32 v87, vcc, 0, v71, vcc
	v_add_co_u32_e32 v94, vcc, s7, v70
	s_mov_b32 s7, 0x1c000
	s_nop 0
	v_addc_co_u32_e32 v95, vcc, 0, v71, vcc
	v_add_co_u32_e32 v102, vcc, s7, v70
	s_mov_b32 s7, 0x23000
	s_nop 0
	v_addc_co_u32_e32 v103, vcc, 0, v71, vcc
	v_add_co_u32_e32 v110, vcc, s7, v70
	s_mov_b32 s7, 0x2a000
	s_nop 0
	v_addc_co_u32_e32 v111, vcc, 0, v71, vcc
	v_add_co_u32_e32 v118, vcc, s7, v70
	global_load_dwordx4 v[2:5], v[70:71], off nt
	global_load_dwordx4 v[6:9], v[78:79], off nt
	v_addc_co_u32_e32 v119, vcc, 0, v71, vcc
	global_load_dwordx4 v[10:13], v[86:87], off nt
; __device__ __forceinline__ unsigned cvt_pk_bf16(float lo, float hi) { f32x2_t v = {lo, hi}; bf16x2_t b = __builtin_convertvector(v, bf16x2_t); return __builtin_bit_cast(unsigned, b); }
; __device__ __forceinline__ void conv_span128(const float* W, int ldw, int K, bf16* WT, int rowmode, int kb, int n0, int lane) {
;     const int c = lane & 7, nn = lane >> 3;
;     const float* src = W + (size_t)(kb * 64 + 8 * c) * ldw + n0 + 4 * nn;
;     f32x4 v[4][8];
; #pragma unroll
;     for (int h = 0; h < 4; ++h)
; #pragma unroll
;         for (int i = 0; i < 8; ++i) v[h][i] = __builtin_nontemporal_load((const f32x4*)(src + 32 * h + (size_t)i * ldw));
; #pragma unroll
;     for (int h = 0; h < 4; ++h) {
;         const int n = n0 + 32 * h + 4 * nn; int r = n;
;         if (rowmode == 2) r = ((n >> 7) << 8) + (n & 127);
;         else if (rowmode == 3) r = ((n >> 7) << 8) + 128 + (n & 127);
;         bf16* d0 = WT + (size_t)r * K + kb * 64 + 8 * c;
; #pragma unroll
;         for (int j = 0; j < 4; ++j) { u32x4 o; o.x = cvt_pk_bf16(v[h][0][j], v[h][1][j]); o.y = cvt_pk_bf16(v[h][2][j], v[h][3][j]); o.z = cvt_pk_bf16(v[h][4][j], v[h][5][j]); o.w = cvt_pk_bf16(v[h][6][j], v[h][7][j]);
;             *(u32x4*)(d0 + (size_t)j * K) = o; }
;     }
; }
	global_load_dwordx4 v[14:17], v[94:95], off nt
	global_load_dwordx4 v[18:21], v[102:103], off nt
	global_load_dwordx4 v[22:25], v[110:111], off nt
	global_load_dwordx4 v[26:29], v[118:119], off nt
	s_mov_b32 s7, 0x31000
	v_add_co_u32_e32 v132, vcc, s7, v70
	s_lshl_b32 s7, s13, 7
	s_nop 0
	v_addc_co_u32_e32 v133, vcc, 0, v71, vcc
	global_load_dwordx4 v[30:33], v[132:133], off nt
	global_load_dwordx4 v[34:37], v[70:71], off offset:128 nt
	global_load_dwordx4 v[38:41], v[78:79], off offset:128 nt
	global_load_dwordx4 v[42:45], v[86:87], off offset:128 nt
	global_load_dwordx4 v[46:49], v[94:95], off offset:128 nt
	global_load_dwordx4 v[50:53], v[102:103], off offset:128 nt
	global_load_dwordx4 v[54:57], v[110:111], off offset:128 nt
	global_load_dwordx4 v[58:61], v[118:119], off offset:128 nt
	global_load_dwordx4 v[62:65], v[132:133], off offset:128 nt
	global_load_dwordx4 v[66:69], v[70:71], off offset:256 nt
	s_nop 0
	global_load_dwordx4 v[70:73], v[70:71], off offset:384 nt
	s_nop 0
	global_load_dwordx4 v[74:77], v[78:79], off offset:256 nt
	s_nop 0
	global_load_dwordx4 v[78:81], v[78:79], off offset:384 nt
	s_nop 0
	global_load_dwordx4 v[82:85], v[86:87], off offset:256 nt
	s_nop 0
	global_load_dwordx4 v[86:89], v[86:87], off offset:384 nt
	s_nop 0
	global_load_dwordx4 v[90:93], v[94:95], off offset:256 nt
	s_nop 0
	global_load_dwordx4 v[94:97], v[94:95], off offset:384 nt
	s_nop 0
	global_load_dwordx4 v[98:101], v[102:103], off offset:256 nt
	s_nop 0
	global_load_dwordx4 v[102:105], v[102:103], off offset:384 nt
	s_nop 0
	global_load_dwordx4 v[106:109], v[110:111], off offset:256 nt
	s_nop 0
	global_load_dwordx4 v[110:113], v[110:111], off offset:384 nt
	s_nop 0
	global_load_dwordx4 v[114:117], v[118:119], off offset:256 nt
	s_nop 0
	global_load_dwordx4 v[118:121], v[118:119], off offset:384 nt
	s_nop 0
	global_load_dwordx4 v[122:125], v[132:133], off offset:256 nt
	s_nop 0
	global_load_dwordx4 v[132:135], v[132:133], off offset:384 nt
	s_add_u32 s8, s11, s7
	s_addc_u32 s9, s9, 0
	s_lshl_b32 s6, s6, 1
	v_lshl_or_b32 v136, s10, 7, v128
	v_or_b32_e32 v136, s6, v136
	v_mov_b32_e32 v131, v187
	v_ashrrev_i32_e32 v137, 31, v136
	v_lshl_add_u64 v[130:131], s[8:9], 0, v[130:131]
	v_lshlrev_b64 v[136:137], 12, v[136:137]
	v_lshl_add_u64 v[140:141], v[130:131], 0, v[136:137]
	s_movk_i32 s7, 0x2000
	s_movk_i32 s8, 0x3000
	v_readlane_b32 s41, v255, 8
	v_readlane_b32 s42, v255, 9
	v_readlane_b32 s43, v255, 10
	s_waitcnt vmcnt(30)
	v_cvt_pk_bf16_f32 v136, v2, v6
	v_add_co_u32_e32 v2, vcc, s7, v140
	s_waitcnt vmcnt(28)
	v_cvt_pk_bf16_f32 v137, v10, v14
	s_waitcnt vmcnt(26)
	v_cvt_pk_bf16_f32 v138, v18, v22
	s_waitcnt vmcnt(24)
	v_cvt_pk_bf16_f32 v139, v26, v30
	global_store_dwordx4 v[140:141], v[136:139], off nt
	s_nop 1
	v_cvt_pk_bf16_f32 v136, v3, v7
	v_cvt_pk_bf16_f32 v137, v11, v15
	v_cvt_pk_bf16_f32 v138, v19, v23
	v_cvt_pk_bf16_f32 v139, v27, v31
	v_addc_co_u32_e32 v3, vcc, 0, v141, vcc
	global_store_dwordx4 v[2:3], v[136:139], off offset:-4096 nt
	v_add_co_u32_e32 v6, vcc, s8, v140
	s_nop 0
	v_cvt_pk_bf16_f32 v136, v4, v8
	v_cvt_pk_bf16_f32 v137, v12, v16
	v_cvt_pk_bf16_f32 v138, v20, v24
	v_cvt_pk_bf16_f32 v139, v28, v32
	global_store_dwordx4 v[2:3], v[136:139], off nt
	v_cvt_pk_bf16_f32 v2, v5, v9
	v_cvt_pk_bf16_f32 v3, v13, v17
	v_cvt_pk_bf16_f32 v4, v21, v25
	v_cvt_pk_bf16_f32 v5, v29, v33
	v_addc_co_u32_e32 v7, vcc, 0, v141, vcc
	global_store_dwordx4 v[6:7], v[2:5], off nt
	s_nop 1
	v_or_b32_e32 v2, s12, v128
	v_or_b32_e32 v2, s6, v2
	v_ashrrev_i32_e32 v3, 31, v2
	v_lshlrev_b64 v[2:3], 12, v[2:3]
	v_lshl_add_u64 v[6:7], v[130:131], 0, v[2:3]
	s_waitcnt vmcnt(26)
	v_cvt_pk_bf16_f32 v2, v34, v38
	s_waitcnt vmcnt(24)
	v_cvt_pk_bf16_f32 v3, v42, v46
	s_waitcnt vmcnt(22)
	v_cvt_pk_bf16_f32 v4, v50, v54
	s_waitcnt vmcnt(20)
	v_cvt_pk_bf16_f32 v5, v58, v62
	v_add_co_u32_e32 v8, vcc, s7, v6
	global_store_dwordx4 v[6:7], v[2:5], off nt
	s_nop 0
	v_addc_co_u32_e32 v9, vcc, 0, v7, vcc
	v_cvt_pk_bf16_f32 v2, v35, v39
	v_cvt_pk_bf16_f32 v3, v43, v47
	v_cvt_pk_bf16_f32 v4, v51, v55
	v_cvt_pk_bf16_f32 v5, v59, v63
	global_store_dwordx4 v[8:9], v[2:5], off offset:-4096 nt
	v_add_co_u32_e32 v6, vcc, s8, v6
	s_nop 0
	v_cvt_pk_bf16_f32 v2, v36, v40
	v_cvt_pk_bf16_f32 v3, v44, v48
	v_cvt_pk_bf16_f32 v4, v52, v56
	v_cvt_pk_bf16_f32 v5, v60, v64
	global_store_dwordx4 v[8:9], v[2:5], off nt
	v_addc_co_u32_e32 v7, vcc, 0, v7, vcc
	s_nop 0
	v_cvt_pk_bf16_f32 v2, v37, v41
	v_cvt_pk_bf16_f32 v3, v45, v49
	v_cvt_pk_bf16_f32 v4, v53, v57
	v_cvt_pk_bf16_f32 v5, v61, v65
	global_store_dwordx4 v[6:7], v[2:5], off nt
	s_nop 1
	v_or_b32_e32 v2, s5, v128
	v_or_b32_e32 v2, s6, v2
	v_ashrrev_i32_e32 v3, 31, v2
	v_lshlrev_b64 v[2:3], 12, v[2:3]
	v_lshl_add_u64 v[6:7], v[130:131], 0, v[2:3]
	s_waitcnt vmcnt(21)
	v_cvt_pk_bf16_f32 v2, v66, v74
	s_waitcnt vmcnt(17)
	v_cvt_pk_bf16_f32 v3, v82, v90
	s_waitcnt vmcnt(13)
	v_cvt_pk_bf16_f32 v4, v98, v106
	s_waitcnt vmcnt(9)
	v_cvt_pk_bf16_f32 v5, v114, v122
	v_add_co_u32_e32 v8, vcc, s7, v6
	global_store_dwordx4 v[6:7], v[2:5], off nt
	s_nop 0
	v_addc_co_u32_e32 v9, vcc, 0, v7, vcc
	v_cvt_pk_bf16_f32 v2, v67, v75
	v_cvt_pk_bf16_f32 v3, v83, v91
	v_cvt_pk_bf16_f32 v4, v99, v107
	v_cvt_pk_bf16_f32 v5, v115, v123
	global_store_dwordx4 v[8:9], v[2:5], off offset:-4096 nt
	v_add_co_u32_e32 v6, vcc, s8, v6
	s_nop 0
	v_cvt_pk_bf16_f32 v2, v68, v76
	v_cvt_pk_bf16_f32 v3, v84, v92
	v_cvt_pk_bf16_f32 v4, v100, v108
	v_cvt_pk_bf16_f32 v5, v116, v124
	global_store_dwordx4 v[8:9], v[2:5], off nt
	v_addc_co_u32_e32 v7, vcc, 0, v7, vcc
	s_nop 0
	v_cvt_pk_bf16_f32 v2, v69, v77
	v_cvt_pk_bf16_f32 v3, v85, v93
	v_cvt_pk_bf16_f32 v4, v101, v109
	v_cvt_pk_bf16_f32 v5, v117, v125
	global_store_dwordx4 v[6:7], v[2:5], off nt
	s_nop 1
	v_or_b32_e32 v2, s4, v128
	v_or_b32_e32 v2, s6, v2
	v_ashrrev_i32_e32 v3, 31, v2
	v_lshlrev_b64 v[2:3], 12, v[2:3]
	v_lshl_add_u64 v[6:7], v[130:131], 0, v[2:3]
	v_cvt_pk_bf16_f32 v2, v70, v78
	v_cvt_pk_bf16_f32 v3, v86, v94
	v_cvt_pk_bf16_f32 v4, v102, v110
	s_waitcnt vmcnt(12)
	v_cvt_pk_bf16_f32 v5, v118, v132
	v_add_co_u32_e32 v8, vcc, s7, v6
	global_store_dwordx4 v[6:7], v[2:5], off nt
	s_nop 0
	v_addc_co_u32_e32 v9, vcc, 0, v7, vcc
	v_cvt_pk_bf16_f32 v2, v71, v79
	v_cvt_pk_bf16_f32 v3, v87, v95
	v_cvt_pk_bf16_f32 v4, v103, v111
	v_cvt_pk_bf16_f32 v5, v119, v133
	global_store_dwordx4 v[8:9], v[2:5], off offset:-4096 nt
	v_add_co_u32_e32 v6, vcc, 0x3000, v6
	s_nop 0
	v_cvt_pk_bf16_f32 v2, v72, v80
	v_cvt_pk_bf16_f32 v3, v88, v96
	v_cvt_pk_bf16_f32 v4, v104, v112
	v_cvt_pk_bf16_f32 v5, v120, v134
	global_store_dwordx4 v[8:9], v[2:5], off nt
	v_addc_co_u32_e32 v7, vcc, 0, v7, vcc
	s_nop 0
	v_cvt_pk_bf16_f32 v2, v73, v81
	v_cvt_pk_bf16_f32 v3, v89, v97
	v_cvt_pk_bf16_f32 v4, v105, v113
	v_cvt_pk_bf16_f32 v5, v121, v135
	global_store_dwordx4 v[6:7], v[2:5], off nt
	s_branch .LBB0_1065
